# scan LDS images stored with bit-6 flipped rows so the recurrence waves' a/b operand reads are bank-conflict free; b read with four ds_read_b32 immediates (no per-step address bump)
# baseline (speedup 1.0000x reference)
.LBB0_779:
	s_or_b64 exec, exec, s[0:1]
	v_lshlrev_b64 v[2:3], 11, v[126:127]
	v_lshl_add_u64 v[4:5], s[66:67], 0, v[2:3]
	v_lshlrev_b64 v[6:7], 1, v[0:1]
	v_lshl_add_u64 v[4:5], v[4:5], 0, v[6:7]
	global_load_dwordx4 v[40:43], v[4:5], off nt
	v_lshlrev_b64 v[4:5], 12, v[126:127]
	v_lshl_add_u64 v[2:3], s[68:69], 0, v[2:3]
	v_lshl_add_u64 v[4:5], s[64:65], 0, v[4:5]
	s_waitcnt vmcnt(3)
	v_and_b32_e32 v15, 0xffff0000, v16
	v_lshlrev_b32_e32 v60, 16, v17
	v_and_b32_e32 v61, 0xffff0000, v17
	s_waitcnt vmcnt(2)
	v_lshlrev_b32_e32 v62, 16, v20
	v_and_b32_e32 v63, 0xffff0000, v20
	v_lshlrev_b32_e32 v68, 16, v21
	v_and_b32_e32 v69, 0xffff0000, v21
	v_and_b32_e32 v10, 0xffff0000, v28
	v_lshlrev_b32_e32 v11, 16, v29
	v_and_b32_e32 v12, 0xffff0000, v29
	v_lshlrev_b32_e32 v13, 16, v32
	v_and_b32_e32 v44, 0xffff0000, v32
	v_lshlrev_b32_e32 v45, 16, v33
	v_and_b32_e32 v46, 0xffff0000, v33
	v_mov_b32_e32 v48, v124
	v_add_u32_e32 v49, s3, v115
	s_add_i32 s0, 0, 0x20c00
	s_add_i32 s1, 0, 0x20d00
	v_lshl_add_u64 v[2:3], v[2:3], 0, v[6:7]
	v_lshl_add_u64 v[0:1], v[0:1], 2, v[4:5]
	v_lshlrev_b32_e32 v14, 16, v16
	v_lshlrev_b32_e32 v9, 16, v28
	s_add_i32 s2, 0, 0x20e00
	v_add_u32_e32 v50, s0, v115
	v_add_u32_e32 v51, s1, v115
	v_sub_f32_e32 v75, v10, v15
	v_sub_f32_e32 v77, v12, v61
	v_sub_f32_e32 v76, v11, v60
	v_sub_f32_e32 v83, v44, v63
	v_sub_f32_e32 v82, v13, v62
	v_sub_f32_e32 v87, v46, v69
	v_sub_f32_e32 v86, v45, v68
	global_load_dwordx4 v[44:47], v[2:3], off nt
	global_load_dwordx4 v[4:7], v[0:1], off offset:16 nt
	s_nop 0
	global_load_dwordx4 v[0:3], v[0:1], off nt
	ds_read_b128 v[10:13], v49
	v_sub_f32_e32 v74, v9, v14
	v_add_u32_e32 v9, s2, v115
	ds_read_b128 v[52:55], v50
	ds_read_b128 v[48:51], v51
	ds_read_b128 v[56:59], v9
	v_or_b32_e32 v120, 16, v115
	v_add_u32_e32 v103, s3, v120
	s_waitcnt lgkmcnt(3)
	v_pk_fma_f32 v[80:81], v[10:11], v[74:75], v[14:15]
	s_waitcnt lgkmcnt(2)
	v_pk_fma_f32 v[14:15], v[86:87], v[54:55], v[68:69]
	v_pk_fma_f32 v[68:69], v[82:83], v[52:53], v[62:63]
	v_add_u32_e32 v104, s0, v120
	v_pk_fma_f32 v[78:79], v[12:13], v[76:77], v[60:61]
	s_waitcnt lgkmcnt(0)
	v_pk_mul_f32 v[74:75], v[14:15], v[58:59]
	v_pk_mul_f32 v[76:77], v[68:69], v[56:57]
	ds_read_b128 v[52:55], v103
	ds_read_b128 v[56:59], v104
	v_add_u32_e32 v9, s1, v120
	v_add_u32_e32 v60, s2, v120
	ds_read_b128 v[10:13], v9
	ds_read_b128 v[60:63], v60
	v_lshlrev_b32_e32 v70, 16, v22
	v_and_b32_e32 v71, 0xffff0000, v22
	v_lshlrev_b32_e32 v96, 16, v34
	v_and_b32_e32 v97, 0xffff0000, v34
	v_lshlrev_b32_e32 v72, 16, v23
	v_and_b32_e32 v73, 0xffff0000, v23
	v_lshlrev_b32_e32 v98, 16, v35
	v_and_b32_e32 v99, 0xffff0000, v35
	v_sub_f32_e32 v83, v97, v71
	v_sub_f32_e32 v82, v96, v70
	v_sub_f32_e32 v87, v99, v73
	v_sub_f32_e32 v86, v98, v72
	s_waitcnt lgkmcnt(2)
	v_pk_fma_f32 v[56:57], v[82:83], v[56:57], v[70:71]
	v_pk_fma_f32 v[58:59], v[86:87], v[58:59], v[72:73]
	s_waitcnt lgkmcnt(0)
	v_pk_mul_f32 v[98:99], v[56:57], v[60:61]
	v_pk_mul_f32 v[96:97], v[58:59], v[62:63]
	v_mov_b32_e32 v62, v77
	v_mov_b32_e32 v63, v99
	v_mov_b32_e32 v60, v76
	v_mov_b32_e32 v61, v98
	v_pk_mul_f32 v[62:63], v[62:63], v[62:63]
	v_mov_b32_e32 v70, v75
	v_mov_b32_e32 v71, v97
	v_pk_fma_f32 v[60:61], v[60:61], v[60:61], v[62:63]
	v_mov_b32_e32 v62, v74
	v_mov_b32_e32 v63, v96
	v_pk_mul_f32 v[70:71], v[70:71], v[70:71]
	s_mov_b32 s0, 0xf800000
	v_pk_fma_f32 v[62:63], v[62:63], v[62:63], v[70:71]
	v_lshlrev_b32_e32 v64, 16, v18
	v_pk_add_f32 v[60:61], v[60:61], v[62:63]
	v_and_b32_e32 v65, 0xffff0000, v18
	v_add_f32_e32 v9, v60, v61
	v_lshlrev_b32_e32 v84, 16, v30
	v_and_b32_e32 v100, 0xffff0000, v30
	v_add_f32_dpp v9, v9, v9 row_half_mirror row_mask:0xf bank_mask:0xf bound_ctrl:1
	v_sub_f32_e32 v61, v100, v65
	v_lshlrev_b32_e32 v66, 16, v19
	v_add_f32_dpp v9, v9, v9 quad_perm:[3,2,1,0] row_mask:0xf bank_mask:0xf bound_ctrl:1
	v_and_b32_e32 v67, 0xffff0000, v19
	v_lshlrev_b32_e32 v101, 16, v31
	v_add_f32_dpp v9, v9, v9 quad_perm:[1,0,3,2] row_mask:0xf bank_mask:0xf bound_ctrl:1
	v_mul_f32_e32 v60, 0x4f800000, v9
	v_cmp_gt_f32_e32 vcc, s0, v9
	v_and_b32_e32 v102, 0xffff0000, v31
	v_sub_f32_e32 v63, v102, v67
	v_cndmask_b32_e32 v9, v9, v60, vcc
	v_sqrt_f32_e32 v62, v9
	v_sub_f32_e32 v60, v84, v64
	v_pk_fma_f32 v[72:73], v[60:61], v[52:53], v[64:65]
	s_waitcnt vmcnt(3)
	v_lshlrev_b32_e32 v88, 16, v40
	v_add_u32_e32 v70, -1, v62
	v_fma_f32 v71, -v70, v62, v9
	v_cmp_ge_f32_e64 s[0:1], 0, v71
	v_add_u32_e32 v71, 1, v62
	v_and_b32_e32 v89, 0xffff0000, v40
	v_cndmask_b32_e64 v70, v62, v70, s[0:1]
	v_fma_f32 v62, -v71, v62, v9
	v_cmp_lt_f32_e64 s[0:1], 0, v62
	v_lshlrev_b32_e32 v90, 16, v41
	v_and_b32_e32 v91, 0xffff0000, v41
	v_cndmask_b32_e64 v62, v70, v71, s[0:1]
	v_mul_f32_e32 v70, 0x37800000, v62
	v_cndmask_b32_e32 v62, v62, v70, vcc
	v_mov_b32_e32 v70, 0x260
	v_cmp_class_f32_e32 vcc, v9, v70
	v_pk_add_f32 v[60:61], v[88:89], -1.0 op_sel_hi:[1,0]
	v_lshlrev_b32_e32 v92, 16, v42
	v_cndmask_b32_e32 v9, v62, v9, vcc
	v_max_f32_e32 v9, 0x2b8cbccc, v9
	v_div_scale_f32 v82, s[0:1], v9, v9, 1.0
	v_rcp_f32_e32 v83, v82
	v_sub_f32_e32 v62, v101, v66
	v_pk_fma_f32 v[70:71], v[62:63], v[54:55], v[66:67]
	s_add_i32 s0, 0, 0x20f00
	v_fma_f32 v52, -v82, v83, 1.0
	v_fmac_f32_e32 v83, v52, v83
	v_div_scale_f32 v52, vcc, 1.0, v9, 1.0
	v_mul_f32_e32 v53, v52, v83
	v_fma_f32 v54, -v82, v53, v52
	v_fmac_f32_e32 v53, v54, v83
	v_fma_f32 v52, -v82, v53, v52
	v_div_fmas_f32 v52, v52, v83, v53
	v_div_fixup_f32 v84, v52, v9, 1.0
	v_add_u32_e32 v9, s0, v115
	ds_read_b128 v[52:55], v9
	s_add_i32 s1, 0, 0x21000
	v_pk_add_f32 v[62:63], v[90:91], -1.0 op_sel_hi:[1,0]
	v_add_u32_e32 v9, s1, v115
	v_pk_mul_f32 v[82:83], v[76:77], v[84:85] op_sel_hi:[1,0]
	v_pk_mul_f32 v[86:87], v[74:75], v[84:85] op_sel_hi:[1,0]
	ds_read_b128 v[74:77], v9
	s_waitcnt lgkmcnt(1)
	v_pk_fma_f32 v[54:55], v[62:63], v[54:55], 1.0 op_sel_hi:[1,1,0]
	v_pk_fma_f32 v[52:53], v[60:61], v[52:53], 1.0 op_sel_hi:[1,1,0]
	v_add_u32_e32 v9, s0, v120
	v_pk_mul_f32 v[62:63], v[14:15], v[54:55]
	v_pk_mul_f32 v[60:61], v[68:69], v[52:53]
	ds_read_b128 v[52:55], v9
	v_and_b32_e32 v93, 0xffff0000, v42
	v_lshlrev_b32_e32 v94, 16, v43
	v_and_b32_e32 v95, 0xffff0000, v43
	v_pk_mul_f32 v[68:69], v[96:97], v[84:85] op_sel_hi:[1,0]
	v_pk_add_f32 v[96:97], v[92:93], -1.0 op_sel_hi:[1,0]
	v_pk_mul_f32 v[14:15], v[98:99], v[84:85] op_sel_hi:[1,0]
	v_pk_add_f32 v[98:99], v[94:95], -1.0 op_sel_hi:[1,0]
	s_waitcnt lgkmcnt(0)
	v_pk_fma_f32 v[52:53], v[96:97], v[52:53], 1.0 op_sel_hi:[1,1,0]
	v_pk_mul_f32 v[64:65], v[82:83], v[88:89]
	v_pk_fma_f32 v[54:55], v[98:99], v[54:55], 1.0 op_sel_hi:[1,1,0]
	v_pk_mul_f32 v[52:53], v[56:57], v[52:53]
	v_pk_mul_f32 v[56:57], v[14:15], v[92:93]
	v_pk_mul_f32 v[66:67], v[86:87], v[90:91]
	v_pk_mul_f32 v[54:55], v[58:59], v[54:55]
	v_pk_mul_f32 v[58:59], v[68:69], v[94:95]
	v_mov_b32_e32 v96, v73
	v_mov_b32_e32 v97, v81
	v_mov_b32_e32 v98, v57
	v_mov_b32_e32 v99, v65
	v_mov_b32_e32 v92, v72
	v_mov_b32_e32 v93, v80
	v_mov_b32_e32 v94, v56
	v_mov_b32_e32 v95, v64
	v_pk_mul_f32 v[96:97], v[96:97], v[98:99]
	v_mov_b32_e32 v98, v71
	v_mov_b32_e32 v99, v79
	v_mov_b32_e32 v104, v59
	v_mov_b32_e32 v105, v67
	v_pk_mul_f32 v[102:103], v[80:81], v[60:61]
	v_add_u32_e32 v9, s1, v120
	v_pk_fma_f32 v[92:93], v[92:93], v[94:95], v[96:97]
	v_mov_b32_e32 v94, v70
	v_mov_b32_e32 v95, v78
	v_mov_b32_e32 v96, v58
	v_mov_b32_e32 v97, v66
	v_pk_mul_f32 v[98:99], v[98:99], v[104:105]
	ds_read_b128 v[88:91], v9
	v_pk_fma_f32 v[94:95], v[94:95], v[96:97], v[98:99]
	v_mov_b32_e32 v97, v74
	v_mov_b32_e32 v99, v102
	v_mov_b32_e32 v74, v81
	v_mov_b32_e32 v102, v61
	v_pk_mul_f32 v[100:101], v[78:79], v[62:63]
	v_mov_b32_e32 v96, v80
	v_mov_b32_e32 v98, v60
	v_pk_mul_f32 v[74:75], v[74:75], v[102:103]
	v_pk_add_f32 v[92:93], v[92:93], v[94:95]
	v_pk_fma_f32 v[74:75], v[96:97], v[98:99], v[74:75]
	v_mov_b32_e32 v97, v76
	v_mov_b32_e32 v99, v100
	v_mov_b32_e32 v76, v79
	v_mov_b32_e32 v100, v63
	v_mov_b32_e32 v96, v78
	v_mov_b32_e32 v98, v62
	v_pk_mul_f32 v[76:77], v[76:77], v[100:101]
	v_pk_mul_f32 v[94:95], v[72:73], v[52:53]
	v_pk_fma_f32 v[76:77], v[96:97], v[98:99], v[76:77]
	v_add_f32_e32 v9, 0, v93
	v_pk_add_f32 v[74:75], v[74:75], v[76:77]
	s_waitcnt lgkmcnt(0)
	v_mov_b32_e32 v77, v88
	v_mov_b32_e32 v97, v94
	v_mov_b32_e32 v88, v73
	v_mov_b32_e32 v94, v53
	v_add_f32_e32 v9, v92, v9
	v_pk_mul_f32 v[92:93], v[70:71], v[54:55]
	v_mov_b32_e32 v76, v72
	v_mov_b32_e32 v96, v52
	v_pk_mul_f32 v[88:89], v[88:89], v[94:95]
	v_mov_b32_e32 v95, v92
	v_pk_fma_f32 v[76:77], v[76:77], v[96:97], v[88:89]
	v_mov_b32_e32 v89, v90
	v_mov_b32_e32 v90, v71
	v_mov_b32_e32 v92, v55
	v_mov_b32_e32 v88, v70
	v_mov_b32_e32 v94, v54
	v_pk_mul_f32 v[90:91], v[90:91], v[92:93]
	v_add_f32_dpp v9, v9, v9 row_half_mirror row_mask:0xf bank_mask:0xf bound_ctrl:1
	v_pk_fma_f32 v[88:89], v[88:89], v[94:95], v[90:91]
	v_lshlrev_b32_e32 v117, 9, v113
	v_add_f32_dpp v9, v9, v9 quad_perm:[3,2,1,0] row_mask:0xf bank_mask:0xf bound_ctrl:1
	v_pk_add_f32 v[76:77], v[76:77], v[88:89]
	v_and_b32_e32 v88, 8, v112
	v_add_f32_dpp v84, v9, v9 quad_perm:[1,0,3,2] row_mask:0xf bank_mask:0xf bound_ctrl:1
	v_and_or_b32 v116, v85, 64, v88
	v_and_b32_e32 v88, 8, v109
	v_pk_add_f32 v[74:75], v[74:75], 0 op_sel_hi:[1,0]
	v_mov_b32_e32 v85, v84
	v_cmp_ne_u32_e32 vcc, 0, v88
	v_add_u32_e32 v88, 0, v117
	v_lshlrev_b32_e32 v118, 8, v113
	v_mov_b32_e32 v104, 0
	v_mov_b32_e32 v105, 0
	v_mov_b32_e32 v106, v8
	v_mov_b32_e32 v107, v8
	v_pk_add_f32 v[74:75], v[74:75], v[76:77]
	v_mov_b32_e32 v76, v8
	v_mov_b32_e32 v77, v8
	v_sub_u32_e32 v122, v88, v118
	s_movk_i32 s0, 0x300
	v_pk_mul_f32 v[98:99], v[82:83], v[84:85] op_sel_hi:[1,0]
	v_pk_mul_f32 v[96:97], v[86:87], v[84:85] op_sel_hi:[1,0]
	s_waitcnt vmcnt(0)
	v_mov_b32_dpp v104, v0 row_shr:8 row_mask:0xf bank_mask:0xf
	v_mov_b32_dpp v105, v1 row_shr:8 row_mask:0xf bank_mask:0xf
	v_mov_b32_dpp v106, v2 row_shr:8 row_mask:0xf bank_mask:0xf
	v_mov_b32_dpp v107, v3 row_shr:8 row_mask:0xf bank_mask:0xf
	v_mov_b32_dpp v76, v74 row_half_mirror row_mask:0xf bank_mask:0xf
	v_mov_b32_dpp v77, v75 row_half_mirror row_mask:0xf bank_mask:0xf
	v_mad_u32_u24 v123, v113, s0, v122
	v_xor_b32_e32 v102, 0x80000000, v82
	v_xor_b32_e32 v103, 0x80000000, v83
	v_xor_b32_e32 v100, 0x80000000, v86
	v_xor_b32_e32 v101, 0x80000000, v87
	v_pk_fma_f32 v[96:97], v[2:3], v[78:79], v[96:97] neg_lo:[0,0,1] neg_hi:[0,0,1]
	v_pk_fma_f32 v[98:99], v[0:1], v[80:81], v[98:99] neg_lo:[0,0,1] neg_hi:[0,0,1]
	v_pk_mul_f32 v[78:79], v[82:83], v[104:105] neg_lo:[1,0] neg_hi:[1,0]
	v_pk_mul_f32 v[80:81], v[86:87], v[106:107] neg_lo:[1,0] neg_hi:[1,0]
	v_cmp_eq_u32_e64 s[0:1], 0, v114
	v_pk_add_f32 v[74:75], v[74:75], v[76:77]
	v_mov_b32_e32 v76, v8
	v_mov_b32_e32 v77, v8
	v_lshlrev_b32_e32 v119, 8, v114
	v_cndmask_b32_e64 v86, v81, v101, s[0:1]
	v_cndmask_b32_e64 v87, v80, v100, s[0:1]
	v_cndmask_b32_e64 v129, v79, v103, s[0:1]
	v_cndmask_b32_e64 v130, v78, v102, s[0:1]
	v_pk_mul_f32 v[78:79], v[98:99], v[104:105]
	v_pk_mul_f32 v[80:81], v[96:97], v[106:107]
	v_mov_b32_dpp v76, v74 quad_perm:[3,2,1,0] row_mask:0xf bank_mask:0xf
	v_mov_b32_dpp v77, v75 quad_perm:[3,2,1,0] row_mask:0xf bank_mask:0xf
	v_add_u32_e32 v121, v88, v119
	v_and_or_b32 v128, v115, 32, v116
	v_cndmask_b32_e64 v81, v81, v97, s[0:1]
	v_cndmask_b32_e64 v131, v80, v96, s[0:1]
	v_cndmask_b32_e64 v80, v79, v99, s[0:1]
	v_cndmask_b32_e64 v132, v78, v98, s[0:1]
	v_mov_b32_e32 v9, v8
	v_pk_add_f32 v[74:75], v[74:75], v[76:77]
	v_mov_b32_e32 v76, 0
	v_mov_b32_e32 v77, 0
	v_mov_b32_e32 v88, 0
	v_mov_b32_e32 v91, 0
	v_mov_b32_e32 v90, 0
	v_mov_b32_e32 v89, 0
	v_mov_b32_e32 v92, 0
	v_mov_b32_e32 v95, 0
	v_mov_b32_e32 v94, 0
	v_mov_b32_e32 v93, 0
	v_cvt_pk_bf16_f32 v78, v130, v129
	v_cvt_pk_bf16_f32 v79, v87, v86
	v_cvt_pk_bf16_f32 v80, v132, v80
	v_cvt_pk_bf16_f32 v81, v131, v81
	v_add_u32_e32 v86, v121, v128
	v_mov_b32_dpp v76, v74 quad_perm:[1,0,3,2] row_mask:0xf bank_mask:0xf
	v_mov_b32_dpp v77, v75 quad_perm:[1,0,3,2] row_mask:0xf bank_mask:0xf
	v_mov_b32_dpp v88, v64 row_shr:8 row_mask:0xf bank_mask:0xf
	v_mov_b32_dpp v91, v60 row_shr:8 row_mask:0xf bank_mask:0xf
	v_mov_b32_dpp v90, v65 row_shr:8 row_mask:0xf bank_mask:0xf
	v_mov_b32_dpp v89, v61 row_shr:8 row_mask:0xf bank_mask:0xf
	v_mov_b32_dpp v92, v66 row_shr:8 row_mask:0xf bank_mask:0xf
	v_mov_b32_dpp v95, v62 row_shr:8 row_mask:0xf bank_mask:0xf
	v_mov_b32_dpp v94, v67 row_shr:8 row_mask:0xf bank_mask:0xf
	v_mov_b32_dpp v93, v63 row_shr:8 row_mask:0xf bank_mask:0xf
	v_lshrrev_b32_e32 v201, 2, v86
	v_bitop3_b32 v201, v201, v86, 64 bitop3:0x6c
	ds_write2_b64 v201, v[78:79], v[80:81] offset1:16
	v_add_u32_e32 v87, v122, v115
	v_add_u32_e32 v86, v123, v115
	v_mov_b64_e32 v[80:81], v[8:9]
	v_mov_b64_e32 v[78:79], v[8:9]
	s_and_saveexec_b64 s[4:5], vcc
	s_cbranch_execz .LBB0_781
	v_pk_mul_f32 v[80:81], v[2:3], v[106:107]
	v_pk_mul_f32 v[78:79], v[0:1], v[104:105]
	ds_write_b128 v87, v[78:81] offset:16384
	v_mov_b32_e32 v78, v92
	v_mov_b32_e32 v79, v94
	v_pk_mul_f32 v[80:81], v[2:3], v[78:79]
	v_mov_b32_e32 v78, v88
	v_mov_b32_e32 v79, v90
	v_pk_mul_f32 v[78:79], v[0:1], v[78:79]
	ds_write_b128 v86, v[78:81] offset:32768
	v_mov_b32_e32 v78, v95
	v_mov_b32_e32 v79, v93
	v_pk_mul_f32 v[80:81], v[2:3], v[78:79]
	v_mov_b32_e32 v78, v91
	v_mov_b32_e32 v79, v89
	v_pk_mul_f32 v[78:79], v[0:1], v[78:79]
	v_xor_b32_e32 v203, 64, v86
	ds_write_b128 v203, v[78:81] offset:33024
	ds_write_b128 v86, v[64:67] offset:33280
	v_xor_b32_e32 v203, 64, v86
	ds_write_b128 v203, v[60:63] offset:33536
	v_pk_mul_f32 v[60:61], v[82:83], v[88:89] neg_lo:[1,0] neg_hi:[1,0]
	v_pk_mul_f32 v[62:63], v[100:101], v[92:93]
	v_pk_fma_f32 v[60:61], v[102:103], v[90:91], v[60:61] op_sel:[1,0,0] op_sel_hi:[0,1,1]
	v_pk_fma_f32 v[62:63], v[100:101], v[94:95], v[62:63] op_sel:[1,0,0] op_sel_hi:[0,1,1]
	v_pk_add_f32 v[60:61], v[60:61], v[62:63]
	v_pk_mul_f32 v[62:63], v[96:97], v[92:93]
	v_pk_add_f32 v[80:81], v[60:61], 0 op_sel_hi:[1,0]
	v_pk_mul_f32 v[60:61], v[98:99], v[88:89]
	v_pk_fma_f32 v[62:63], v[96:97], v[94:95], v[62:63] op_sel:[1,0,0] op_sel_hi:[0,1,1]
	v_pk_fma_f32 v[60:61], v[98:99], v[90:91], v[60:61] op_sel:[1,0,0] op_sel_hi:[0,1,1]
	v_pk_add_f32 v[60:61], v[60:61], v[62:63]
	s_nop 0
	v_pk_add_f32 v[78:79], v[60:61], 0 op_sel_hi:[1,0]
.LBB0_781:
	s_or_b64 exec, exec, s[4:5]
	v_lshlrev_b32_e32 v64, 16, v24
	v_and_b32_e32 v65, 0xffff0000, v24
	v_lshlrev_b32_e32 v66, 16, v25
	v_and_b32_e32 v67, 0xffff0000, v25
	v_lshlrev_b32_e32 v9, 16, v36
	v_and_b32_e32 v82, 0xffff0000, v36
	v_lshlrev_b32_e32 v88, 16, v37
	v_and_b32_e32 v89, 0xffff0000, v37
	s_add_i32 s2, 0, 0x14000
	v_sub_f32_e32 v83, v82, v65
	v_sub_f32_e32 v82, v9, v64
	v_sub_f32_e32 v89, v89, v67
	v_sub_f32_e32 v88, v88, v66
	v_add_u32_e32 v9, s2, v166
	s_add_i32 s2, 0, 0x1a000
	v_pk_fma_f32 v[50:51], v[88:89], v[50:51], v[66:67]
	v_pk_fma_f32 v[48:49], v[82:83], v[48:49], v[64:65]
	v_add_u32_e32 v64, s2, v166
	v_add_u32_e32 v9, v9, v115
	ds_write_b128 v9, v[48:51]
	v_add_u32_e32 v88, v64, v115
	v_mov_b32_e32 v48, v84
	v_mov_b32_e32 v49, v84
	v_pk_mul_f32 v[64:65], v[14:15], v[84:85]
	v_mov_b32_e32 v82, 0
	v_mov_b32_e32 v83, 0
	v_mov_b32_e32 v84, v8
	v_mov_b32_e32 v85, v8
	v_pk_mul_f32 v[66:67], v[68:69], v[48:49]
	v_mov_b32_dpp v82, v4 row_shr:8 row_mask:0xf bank_mask:0xf
	v_mov_b32_dpp v83, v5 row_shr:8 row_mask:0xf bank_mask:0xf
	v_mov_b32_dpp v84, v6 row_shr:8 row_mask:0xf bank_mask:0xf
	v_mov_b32_dpp v85, v7 row_shr:8 row_mask:0xf bank_mask:0xf
	v_xor_b32_e32 v91, 0x80000000, v69
	v_xor_b32_e32 v90, 0x80000000, v68
	v_xor_b32_e32 v89, 0x80000000, v14
	v_xor_b32_e32 v92, 0x80000000, v15
	v_pk_fma_f32 v[64:65], v[4:5], v[72:73], v[64:65] neg_lo:[0,0,1] neg_hi:[0,0,1]
	v_pk_fma_f32 v[66:67], v[6:7], v[70:71], v[66:67] neg_lo:[0,0,1] neg_hi:[0,0,1]
	v_pk_mul_f32 v[70:71], v[90:91], v[84:85]
	v_pk_mul_f32 v[72:73], v[14:15], v[82:83] neg_lo:[1,0] neg_hi:[1,0]
	v_lshlrev_b32_e32 v60, 16, v44
	v_and_b32_e32 v61, 0xffff0000, v44
	v_lshlrev_b32_e32 v62, 16, v45
	v_and_b32_e32 v63, 0xffff0000, v45
	v_cndmask_b32_e64 v91, v71, v91, s[0:1]
	v_cndmask_b32_e64 v90, v70, v90, s[0:1]
	v_cndmask_b32_e64 v92, v73, v92, s[0:1]
	v_cndmask_b32_e64 v89, v72, v89, s[0:1]
	v_pk_mul_f32 v[70:71], v[64:65], v[82:83]
	v_pk_mul_f32 v[72:73], v[66:67], v[84:85]
	ds_write_b128 v88, v[60:63]
	v_mov_b32_e32 v48, 0
	v_mov_b32_e32 v51, 0
	v_mov_b32_e32 v50, 0
	v_mov_b32_e32 v49, 0
	v_mov_b32_e32 v60, 0
	v_mov_b32_e32 v63, 0
	v_mov_b32_e32 v62, 0
	v_and_or_b32 v61, v120, 48, v116
	v_cndmask_b32_e64 v73, v73, v67, s[0:1]
	v_cndmask_b32_e64 v93, v72, v66, s[0:1]
	v_cndmask_b32_e64 v72, v71, v65, s[0:1]
	v_cndmask_b32_e64 v94, v70, v64, s[0:1]
	v_mov_b32_dpp v48, v56 row_shr:8 row_mask:0xf bank_mask:0xf
	v_mov_b32_dpp v51, v52 row_shr:8 row_mask:0xf bank_mask:0xf
	v_mov_b32_dpp v50, v57 row_shr:8 row_mask:0xf bank_mask:0xf
	v_mov_b32_dpp v49, v53 row_shr:8 row_mask:0xf bank_mask:0xf
	v_mov_b32_dpp v60, v58 row_shr:8 row_mask:0xf bank_mask:0xf
	v_mov_b32_dpp v63, v54 row_shr:8 row_mask:0xf bank_mask:0xf
	v_mov_b32_dpp v62, v59 row_shr:8 row_mask:0xf bank_mask:0xf
	v_mov_b32_dpp v8, v55 row_shr:8 row_mask:0xf bank_mask:0xf
	v_cvt_pk_bf16_f32 v70, v89, v92
	v_cvt_pk_bf16_f32 v71, v90, v91
	v_cvt_pk_bf16_f32 v72, v94, v72
	v_cvt_pk_bf16_f32 v73, v93, v73
	v_add_u32_e32 v61, v121, v61
	v_lshrrev_b32_e32 v201, 2, v61
	v_bitop3_b32 v201, v201, v61, 64 bitop3:0x6c
	ds_write2_b64 v201, v[70:71], v[72:73] offset1:16
	s_and_saveexec_b64 s[0:1], vcc
	s_cbranch_execz .LBB0_783
	v_pk_mul_f32 v[72:73], v[6:7], v[84:85]
	v_pk_mul_f32 v[70:71], v[4:5], v[82:83]
	ds_write_b128 v87, v[70:73] offset:16400
	v_mov_b32_e32 v70, v60
	v_mov_b32_e32 v71, v62
	v_pk_mul_f32 v[72:73], v[6:7], v[70:71]
	v_mov_b32_e32 v70, v48
	v_mov_b32_e32 v71, v50
	v_pk_mul_f32 v[70:71], v[4:5], v[70:71]
	ds_write_b128 v86, v[70:73] offset:32784
	v_mov_b32_e32 v70, v63
	v_mov_b32_e32 v71, v8
	v_pk_mul_f32 v[72:73], v[6:7], v[70:71]
	v_mov_b32_e32 v70, v51
	v_mov_b32_e32 v71, v49
	v_pk_mul_f32 v[70:71], v[4:5], v[70:71]
	v_mov_b32_e32 v61, v8
	v_xor_b32_e32 v203, 64, v86
	ds_write_b128 v203, v[70:73] offset:33040
	ds_write_b128 v86, v[56:59] offset:33296
	v_xor_b32_e32 v203, 64, v86
	ds_write_b128 v203, v[52:55] offset:33552
	v_xor_b32_e32 v53, 0x80000000, v69
	v_xor_b32_e32 v52, 0x80000000, v68
	v_xor_b32_e32 v55, 0x80000000, v15
	v_xor_b32_e32 v54, 0x80000000, v14
	v_pk_mul_f32 v[14:15], v[14:15], v[48:49] neg_lo:[1,0] neg_hi:[1,0]
	s_nop 0
	v_pk_fma_f32 v[14:15], v[54:55], v[50:51], v[14:15] op_sel:[1,0,0] op_sel_hi:[0,1,1]
	v_pk_mul_f32 v[54:55], v[52:53], v[60:61]
	s_nop 0
	v_pk_fma_f32 v[52:53], v[52:53], v[62:63], v[54:55] op_sel:[1,0,0] op_sel_hi:[0,1,1]
	v_pk_add_f32 v[14:15], v[14:15], v[52:53]
	s_nop 0
	v_pk_add_f32 v[80:81], v[80:81], v[14:15]
	v_pk_mul_f32 v[14:15], v[64:65], v[48:49]
	v_pk_mul_f32 v[48:49], v[66:67], v[60:61]
	v_pk_fma_f32 v[14:15], v[64:65], v[50:51], v[14:15] op_sel:[1,0,0] op_sel_hi:[0,1,1]
	v_pk_fma_f32 v[48:49], v[66:67], v[62:63], v[48:49] op_sel:[1,0,0] op_sel_hi:[0,1,1]
	v_pk_add_f32 v[14:15], v[14:15], v[48:49]
	s_nop 0
	v_pk_add_f32 v[78:79], v[78:79], v[14:15]

.LBB0_796:
	s_andn2_b64 vcc, exec, s[14:15]
	s_mov_b32 s2, 64
	s_cbranch_vccnz .LBB0_805
	v_mov_b32_e32 v100, v124
	v_add_u32_e32 v108, s46, v167
	v_add_u32_e32 v100, s3, v167
	ds_read_b128 v[100:103], v100
	ds_read_b128 v[108:111], v108
	s_waitcnt vmcnt(9)
	v_lshlrev_b32_e32 v104, 16, v72
	v_and_b32_e32 v105, 0xffff0000, v72
	v_lshlrev_b32_e32 v106, 16, v73
	v_and_b32_e32 v107, 0xffff0000, v73
	s_waitcnt vmcnt(6)
	v_lshlrev_b32_e32 v49, 16, v80
	v_and_b32_e32 v122, 0xffff0000, v80
	v_lshlrev_b32_e32 v120, 16, v81
	v_and_b32_e32 v121, 0xffff0000, v81
	v_add_u32_e32 v146, s47, v167
	v_sub_f32_e32 v121, v121, v107
	v_sub_f32_e32 v120, v120, v106
	v_sub_f32_e32 v123, v122, v105
	v_sub_f32_e32 v122, v49, v104
	s_waitcnt lgkmcnt(1)
	v_pk_fma_f32 v[138:139], v[122:123], v[100:101], v[104:105]
	v_pk_fma_f32 v[140:141], v[120:121], v[102:103], v[106:107]
	v_add_u32_e32 v49, s48, v167
	ds_read_b128 v[104:107], v146
	ds_read_b128 v[100:103], v49
	v_lshlrev_b32_e32 v116, 16, v68
	v_and_b32_e32 v117, 0xffff0000, v68
	s_waitcnt vmcnt(5)
	v_lshlrev_b32_e32 v142, 16, v88
	v_and_b32_e32 v143, 0xffff0000, v88
	v_lshlrev_b32_e32 v118, 16, v69
	v_and_b32_e32 v119, 0xffff0000, v69
	v_lshlrev_b32_e32 v144, 16, v89
	v_and_b32_e32 v145, 0xffff0000, v89
	v_sub_f32_e32 v123, v143, v117
	v_sub_f32_e32 v122, v142, v116
	v_sub_f32_e32 v121, v145, v119
	v_sub_f32_e32 v120, v144, v118
	s_waitcnt lgkmcnt(2)
	v_pk_fma_f32 v[144:145], v[122:123], v[108:109], v[116:117]
	v_add_u32_e32 v49, s3, v168
	v_pk_fma_f32 v[146:147], v[120:121], v[110:111], v[118:119]
	s_waitcnt lgkmcnt(0)
	v_pk_mul_f32 v[142:143], v[144:145], v[100:101]
	v_add_u32_e32 v100, s46, v168
	ds_read_b128 v[108:111], v49
	ds_read_b128 v[116:119], v100
	v_add_u32_e32 v49, s47, v168
	v_add_u32_e32 v120, s48, v168
	v_pk_mul_f32 v[148:149], v[146:147], v[102:103]
	ds_read_b128 v[100:103], v49
	ds_read_b128 v[120:123], v120
	v_lshlrev_b32_e32 v130, 16, v70
	v_and_b32_e32 v131, 0xffff0000, v70
	v_lshlrev_b32_e32 v152, 16, v90
	v_and_b32_e32 v153, 0xffff0000, v90
	v_lshlrev_b32_e32 v134, 16, v71
	v_and_b32_e32 v135, 0xffff0000, v71
	v_lshlrev_b32_e32 v150, 16, v91
	v_and_b32_e32 v151, 0xffff0000, v91
	v_sub_f32_e32 v153, v153, v131
	v_sub_f32_e32 v152, v152, v130
	v_sub_f32_e32 v151, v151, v135
	v_sub_f32_e32 v150, v150, v134
	s_waitcnt lgkmcnt(2)
	v_pk_fma_f32 v[152:153], v[152:153], v[116:117], v[130:131]
	v_pk_fma_f32 v[150:151], v[150:151], v[118:119], v[134:135]
	s_waitcnt lgkmcnt(0)
	v_pk_mul_f32 v[156:157], v[152:153], v[120:121]
	v_pk_mul_f32 v[154:155], v[150:151], v[122:123]
	v_mov_b32_e32 v118, v143
	v_mov_b32_e32 v119, v157
	v_mov_b32_e32 v116, v142
	v_mov_b32_e32 v117, v156
	v_pk_mul_f32 v[118:119], v[118:119], v[118:119]
	v_mov_b32_e32 v120, v149
	v_mov_b32_e32 v121, v155
	v_pk_fma_f32 v[116:117], v[116:117], v[116:117], v[118:119]
	v_mov_b32_e32 v118, v148
	v_mov_b32_e32 v119, v154
	v_pk_mul_f32 v[120:121], v[120:121], v[120:121]
	s_mov_b32 s2, 0xf800000
	v_pk_fma_f32 v[118:119], v[118:119], v[118:119], v[120:121]
	v_lshlrev_b32_e32 v128, 16, v74
	v_pk_add_f32 v[116:117], v[116:117], v[118:119]
	v_and_b32_e32 v129, 0xffff0000, v74
	v_add_f32_e32 v49, v116, v117
	v_lshlrev_b32_e32 v158, 16, v82
	v_and_b32_e32 v159, 0xffff0000, v82
	v_add_f32_dpp v49, v49, v49 row_half_mirror row_mask:0xf bank_mask:0xf bound_ctrl:1
	v_sub_f32_e32 v119, v159, v129
	v_lshlrev_b32_e32 v132, 16, v75
	v_add_f32_dpp v49, v49, v49 quad_perm:[3,2,1,0] row_mask:0xf bank_mask:0xf bound_ctrl:1
	v_and_b32_e32 v133, 0xffff0000, v75
	v_lshlrev_b32_e32 v160, 16, v83
	v_add_f32_dpp v49, v49, v49 quad_perm:[1,0,3,2] row_mask:0xf bank_mask:0xf bound_ctrl:1
	v_mul_f32_e32 v116, 0x4f800000, v49
	v_cmp_gt_f32_e32 vcc, s2, v49
	v_and_b32_e32 v161, 0xffff0000, v83
	v_sub_f32_e32 v117, v161, v133
	v_cndmask_b32_e32 v49, v49, v116, vcc
	v_sqrt_f32_e32 v118, v49
	v_sub_f32_e32 v116, v160, v132
	s_waitcnt vmcnt(3)
	v_lshlrev_b32_e32 v50, 16, v92
	v_and_b32_e32 v51, 0xffff0000, v92
	v_add_u32_e32 v120, -1, v118
	v_fma_f32 v121, -v120, v118, v49
	v_cmp_ge_f32_e64 s[14:15], 0, v121
	v_add_u32_e32 v121, 1, v118
	v_lshlrev_b32_e32 v136, 16, v93
	v_cndmask_b32_e64 v120, v118, v120, s[14:15]
	v_fma_f32 v118, -v121, v118, v49
	v_cmp_lt_f32_e64 s[14:15], 0, v118
	v_and_b32_e32 v137, 0xffff0000, v93
	v_lshlrev_b32_e32 v112, 16, v94
	v_cndmask_b32_e64 v118, v120, v121, s[14:15]
	v_mul_f32_e32 v120, 0x37800000, v118
	v_cndmask_b32_e32 v118, v118, v120, vcc
	v_cmp_class_f32_e32 vcc, v49, v192
	v_and_b32_e32 v113, 0xffff0000, v94
	v_lshlrev_b32_e32 v114, 16, v95
	v_cndmask_b32_e32 v49, v118, v49, vcc
	v_max_f32_e32 v49, 0x2b8cbccc, v49
	v_div_scale_f32 v120, s[14:15], v49, v49, 1.0
	v_rcp_f32_e32 v121, v120
	v_sub_f32_e32 v118, v158, v128
	v_pk_fma_f32 v[130:131], v[118:119], v[108:109], v[128:129]
	v_pk_fma_f32 v[128:129], v[116:117], v[110:111], v[132:133]
	v_fma_f32 v108, -v120, v121, 1.0
	v_fmac_f32_e32 v121, v108, v121
	v_div_scale_f32 v108, vcc, 1.0, v49, 1.0
	v_mul_f32_e32 v109, v108, v121
	v_fma_f32 v110, -v120, v109, v108
	v_fmac_f32_e32 v109, v110, v121
	v_fma_f32 v108, -v120, v109, v108
	v_div_fmas_f32 v108, v108, v121, v109
	v_div_fixup_f32 v158, v108, v49, 1.0
	v_add_u32_e32 v49, s49, v167
	ds_read_b128 v[108:111], v49
	v_pk_add_f32 v[116:117], v[50:51], -1.0 op_sel_hi:[1,0]
	v_pk_add_f32 v[118:119], v[136:137], -1.0 op_sel_hi:[1,0]
	v_add_u32_e32 v49, s50, v167
	ds_read_b128 v[132:135], v49
	s_waitcnt lgkmcnt(1)
	v_pk_fma_f32 v[110:111], v[118:119], v[110:111], 1.0 op_sel_hi:[1,1,0]
	v_pk_fma_f32 v[108:109], v[116:117], v[108:109], 1.0 op_sel_hi:[1,1,0]
	v_add_u32_e32 v49, s49, v168
	v_pk_mul_f32 v[118:119], v[146:147], v[110:111]
	v_pk_mul_f32 v[116:117], v[144:145], v[108:109]
	ds_read_b128 v[108:111], v49
	v_pk_mul_f32 v[142:143], v[142:143], v[158:159] op_sel_hi:[1,0]
	v_and_b32_e32 v115, 0xffff0000, v95
	v_pk_mul_f32 v[194:195], v[148:149], v[158:159] op_sel_hi:[1,0]
	v_pk_mul_f32 v[120:121], v[142:143], v[50:51]
	v_pk_mul_f32 v[50:51], v[156:157], v[158:159] op_sel_hi:[1,0]
	v_pk_add_f32 v[144:145], v[112:113], -1.0 op_sel_hi:[1,0]
	v_pk_mul_f32 v[122:123], v[194:195], v[136:137]
	v_pk_mul_f32 v[136:137], v[154:155], v[158:159] op_sel_hi:[1,0]
	v_pk_add_f32 v[154:155], v[114:115], -1.0 op_sel_hi:[1,0]
	s_waitcnt lgkmcnt(0)
	v_pk_fma_f32 v[108:109], v[144:145], v[108:109], 1.0 op_sel_hi:[1,1,0]
	v_pk_mul_f32 v[112:113], v[50:51], v[112:113]
	v_pk_fma_f32 v[110:111], v[154:155], v[110:111], 1.0 op_sel_hi:[1,1,0]
	v_pk_mul_f32 v[108:109], v[152:153], v[108:109]
	v_pk_mul_f32 v[114:115], v[136:137], v[114:115]
	v_mov_b32_e32 v152, v131
	v_mov_b32_e32 v153, v139
	v_mov_b32_e32 v154, v113
	v_mov_b32_e32 v155, v121
	v_pk_mul_f32 v[110:111], v[150:151], v[110:111]
	v_mov_b32_e32 v144, v130
	v_mov_b32_e32 v145, v138
	v_mov_b32_e32 v150, v112
	v_mov_b32_e32 v151, v120
	v_pk_mul_f32 v[152:153], v[152:153], v[154:155]
	v_mov_b32_e32 v154, v129
	v_mov_b32_e32 v155, v141
	v_mov_b32_e32 v156, v115
	v_mov_b32_e32 v157, v123
	v_pk_mul_f32 v[162:163], v[138:139], v[116:117]
	v_add_u32_e32 v49, s50, v168
	v_pk_fma_f32 v[144:145], v[144:145], v[150:151], v[152:153]
	v_mov_b32_e32 v150, v128
	v_mov_b32_e32 v151, v140
	v_mov_b32_e32 v152, v114
	v_mov_b32_e32 v153, v122
	v_pk_mul_f32 v[154:155], v[154:155], v[156:157]
	ds_read_b128 v[146:149], v49
	v_pk_fma_f32 v[150:151], v[150:151], v[152:153], v[154:155]
	v_mov_b32_e32 v155, v132
	v_mov_b32_e32 v157, v162
	v_mov_b32_e32 v132, v139
	v_mov_b32_e32 v162, v117
	v_pk_mul_f32 v[160:161], v[140:141], v[118:119]
	v_mov_b32_e32 v154, v138
	v_mov_b32_e32 v156, v116
	v_pk_mul_f32 v[132:133], v[132:133], v[162:163]
	v_pk_mul_f32 v[152:153], v[130:131], v[108:109]
	v_pk_fma_f32 v[132:133], v[154:155], v[156:157], v[132:133]
	v_pk_mov_b32 v[154:155], v[140:141], v[134:135] op_sel:[1,0]
	v_pk_mov_b32 v[156:157], v[118:119], v[160:161] op_sel:[1,0]
	v_mov_b32_e32 v134, v140
	v_mov_b32_e32 v160, v118
	v_pk_mul_f32 v[134:135], v[134:135], v[160:161]
	v_pk_add_f32 v[144:145], v[144:145], v[150:151]
	v_pk_fma_f32 v[134:135], v[154:155], v[156:157], v[134:135]
	v_mov_b32_e32 v155, v152
	v_pk_add_f32 v[132:133], v[132:133], v[134:135]
	s_waitcnt lgkmcnt(0)
	v_mov_b32_e32 v135, v146
	v_mov_b32_e32 v146, v131
	v_mov_b32_e32 v152, v109
	v_add_f32_e32 v49, 0, v145
	v_pk_mul_f32 v[150:151], v[128:129], v[110:111]
	v_mov_b32_e32 v134, v130
	v_mov_b32_e32 v154, v108
	v_pk_mul_f32 v[146:147], v[146:147], v[152:153]
	v_add_f32_e32 v49, v144, v49
	v_pk_fma_f32 v[134:135], v[134:135], v[154:155], v[146:147]
	v_pk_mov_b32 v[146:147], v[128:129], v[148:149] op_sel:[1,0]
	v_pk_mov_b32 v[152:153], v[110:111], v[150:151] op_sel:[1,0]
	v_mov_b32_e32 v148, v128
	v_mov_b32_e32 v150, v110
	s_and_b32 s44, s52, 1
	v_add_f32_dpp v49, v49, v49 row_half_mirror row_mask:0xf bank_mask:0xf bound_ctrl:1
	v_pk_mul_f32 v[148:149], v[148:149], v[150:151]
	s_lshl_b32 s2, s44, 13
	v_add_f32_dpp v49, v49, v49 quad_perm:[3,2,1,0] row_mask:0xf bank_mask:0xf bound_ctrl:1
	v_pk_fma_f32 v[146:147], v[146:147], v[152:153], v[148:149]
	v_pk_add_f32 v[132:133], v[132:133], 0 op_sel_hi:[1,0]
	v_add_f32_dpp v144, v49, v49 quad_perm:[1,0,3,2] row_mask:0xf bank_mask:0xf bound_ctrl:1
	v_pk_add_f32 v[134:135], v[134:135], v[146:147]
	v_add_u32_e32 v145, s2, v172
	v_mov_b32_e32 v162, 0
	v_mov_b32_e32 v163, 0
	v_mov_b32_e32 v164, v48
	v_mov_b32_e32 v165, v48
	v_pk_add_f32 v[132:133], v[132:133], v[134:135]
	v_mov_b32_e32 v134, v48
	v_mov_b32_e32 v135, v48
	v_pk_mul_f32 v[156:157], v[142:143], v[144:145] op_sel_hi:[1,0]
	v_pk_mul_f32 v[154:155], v[194:195], v[144:145] op_sel_hi:[1,0]
	s_waitcnt vmcnt(0)
	v_mov_b32_dpp v162, v8 row_shr:8 row_mask:0xf bank_mask:0xf
	v_mov_b32_dpp v163, v9 row_shr:8 row_mask:0xf bank_mask:0xf
	v_mov_b32_dpp v164, v10 row_shr:8 row_mask:0xf bank_mask:0xf
	v_mov_b32_dpp v165, v11 row_shr:8 row_mask:0xf bank_mask:0xf
	v_mov_b32_dpp v134, v132 row_half_mirror row_mask:0xf bank_mask:0xf
	v_mov_b32_dpp v135, v133 row_half_mirror row_mask:0xf bank_mask:0xf
	v_xor_b32_e32 v160, 0x80000000, v142
	v_xor_b32_e32 v161, 0x80000000, v143
	v_xor_b32_e32 v158, 0x80000000, v194
	v_xor_b32_e32 v159, 0x80000000, v195
	v_pk_fma_f32 v[154:155], v[10:11], v[140:141], v[154:155] neg_lo:[0,0,1] neg_hi:[0,0,1]
	v_pk_fma_f32 v[156:157], v[8:9], v[138:139], v[156:157] neg_lo:[0,0,1] neg_hi:[0,0,1]
	v_pk_mul_f32 v[138:139], v[142:143], v[162:163] neg_lo:[1,0] neg_hi:[1,0]
	v_pk_mul_f32 v[140:141], v[194:195], v[164:165] neg_lo:[1,0] neg_hi:[1,0]
	v_pk_add_f32 v[132:133], v[132:133], v[134:135]
	v_mov_b32_e32 v134, v48
	v_mov_b32_e32 v135, v48
	v_cndmask_b32_e64 v194, v141, v159, s[0:1]
	v_cndmask_b32_e64 v195, v140, v158, s[0:1]
	v_cndmask_b32_e64 v197, v139, v161, s[0:1]
	v_cndmask_b32_e64 v198, v138, v160, s[0:1]
	v_pk_mul_f32 v[138:139], v[156:157], v[162:163]
	v_pk_mul_f32 v[140:141], v[154:155], v[164:165]
	v_mov_b32_dpp v134, v132 quad_perm:[3,2,1,0] row_mask:0xf bank_mask:0xf
	v_mov_b32_dpp v135, v133 quad_perm:[3,2,1,0] row_mask:0xf bank_mask:0xf
	v_add_u32_e32 v193, s2, v171
	v_cndmask_b32_e64 v141, v141, v155, s[0:1]
	v_cndmask_b32_e64 v199, v140, v154, s[0:1]
	v_cndmask_b32_e64 v140, v139, v157, s[0:1]
	v_cndmask_b32_e64 v200, v138, v156, s[0:1]
	v_mov_b32_e32 v49, v48
	v_pk_add_f32 v[132:133], v[132:133], v[134:135]
	v_mov_b32_e32 v134, 0
	v_mov_b32_e32 v135, 0
	v_lshl_add_u32 v196, s44, 14, v173
	v_mov_b32_e32 v146, 0
	v_mov_b32_e32 v149, 0
	v_mov_b32_e32 v148, 0
	v_mov_b32_e32 v147, 0
	v_mov_b32_e32 v150, 0
	v_mov_b32_e32 v153, 0
	v_mov_b32_e32 v152, 0
	v_mov_b32_e32 v151, 0
	v_cvt_pk_bf16_f32 v138, v198, v197
	v_cvt_pk_bf16_f32 v139, v195, v194
	v_cvt_pk_bf16_f32 v140, v200, v140
	v_cvt_pk_bf16_f32 v141, v199, v141
	v_add_u32_e32 v194, v193, v183
	v_mov_b32_dpp v134, v132 quad_perm:[1,0,3,2] row_mask:0xf bank_mask:0xf
	v_mov_b32_dpp v135, v133 quad_perm:[1,0,3,2] row_mask:0xf bank_mask:0xf
	v_mov_b32_dpp v146, v120 row_shr:8 row_mask:0xf bank_mask:0xf
	v_mov_b32_dpp v149, v116 row_shr:8 row_mask:0xf bank_mask:0xf
	v_mov_b32_dpp v148, v121 row_shr:8 row_mask:0xf bank_mask:0xf
	v_mov_b32_dpp v147, v117 row_shr:8 row_mask:0xf bank_mask:0xf
	v_mov_b32_dpp v150, v122 row_shr:8 row_mask:0xf bank_mask:0xf
	v_mov_b32_dpp v153, v118 row_shr:8 row_mask:0xf bank_mask:0xf
	v_mov_b32_dpp v152, v123 row_shr:8 row_mask:0xf bank_mask:0xf
	v_mov_b32_dpp v151, v119 row_shr:8 row_mask:0xf bank_mask:0xf
	v_lshrrev_b32_e32 v201, 2, v194
	v_bitop3_b32 v201, v201, v194, 64 bitop3:0x6c
	ds_write2_b64 v201, v[138:139], v[140:141] offset1:16
	v_add_u32_e32 v195, v145, v167
	v_add_u32_e32 v194, v196, v167
	v_mov_b64_e32 v[140:141], v[48:49]
	v_mov_b64_e32 v[138:139], v[48:49]
	s_and_saveexec_b64 s[14:15], s[4:5]
	s_cbranch_execz .LBB0_799
	v_pk_mul_f32 v[140:141], v[10:11], v[164:165]
	v_pk_mul_f32 v[138:139], v[8:9], v[162:163]
	ds_write_b128 v195, v[138:141] offset:16384
	v_mov_b32_e32 v138, v150
	v_mov_b32_e32 v139, v152
	v_pk_mul_f32 v[140:141], v[10:11], v[138:139]
	v_mov_b32_e32 v138, v146
	v_mov_b32_e32 v139, v148
	v_pk_mul_f32 v[138:139], v[8:9], v[138:139]
	ds_write_b128 v194, v[138:141] offset:32768
	v_mov_b32_e32 v138, v153
	v_mov_b32_e32 v139, v151
	v_pk_mul_f32 v[140:141], v[10:11], v[138:139]
	v_mov_b32_e32 v138, v149
	v_mov_b32_e32 v139, v147
	v_pk_mul_f32 v[138:139], v[8:9], v[138:139]
	v_xor_b32_e32 v203, 64, v194
	ds_write_b128 v203, v[138:141] offset:33024
	ds_write_b128 v194, v[120:123] offset:33280
	v_xor_b32_e32 v203, 64, v194
	ds_write_b128 v203, v[116:119] offset:33536
	v_pk_mul_f32 v[116:117], v[142:143], v[146:147] neg_lo:[1,0] neg_hi:[1,0]
	v_pk_mul_f32 v[118:119], v[158:159], v[150:151]
	v_pk_fma_f32 v[116:117], v[160:161], v[148:149], v[116:117] op_sel:[1,0,0] op_sel_hi:[0,1,1]
	v_pk_fma_f32 v[118:119], v[158:159], v[152:153], v[118:119] op_sel:[1,0,0] op_sel_hi:[0,1,1]
	v_pk_add_f32 v[116:117], v[116:117], v[118:119]
	v_pk_mul_f32 v[118:119], v[154:155], v[150:151]
	v_pk_add_f32 v[140:141], v[116:117], 0 op_sel_hi:[1,0]
	v_pk_mul_f32 v[116:117], v[156:157], v[146:147]
	v_pk_fma_f32 v[118:119], v[154:155], v[152:153], v[118:119] op_sel:[1,0,0] op_sel_hi:[0,1,1]
	v_pk_fma_f32 v[116:117], v[156:157], v[148:149], v[116:117] op_sel:[1,0,0] op_sel_hi:[0,1,1]
	v_pk_add_f32 v[116:117], v[116:117], v[118:119]
	s_nop 0
	v_pk_add_f32 v[138:139], v[116:117], 0 op_sel_hi:[1,0]
.LBB0_799:
	s_or_b64 exec, exec, s[14:15]
	s_mul_hi_u32 s2, s52, 0xaaaaaaab
	s_lshr_b32 s2, s2, 1
	s_mul_i32 s2, s2, 3
	v_lshlrev_b32_e32 v120, 16, v76
	v_and_b32_e32 v121, 0xffff0000, v76
	v_lshlrev_b32_e32 v122, 16, v77
	v_and_b32_e32 v123, 0xffff0000, v77
	v_lshlrev_b32_e32 v49, 16, v84
	v_and_b32_e32 v142, 0xffff0000, v84
	v_lshlrev_b32_e32 v146, 16, v85
	v_and_b32_e32 v147, 0xffff0000, v85
	s_sub_i32 s2, s52, s2
	v_sub_f32_e32 v143, v142, v121
	v_sub_f32_e32 v142, v49, v120
	v_sub_f32_e32 v147, v147, v123
	v_sub_f32_e32 v146, v146, v122
	s_lshl_b32 s14, s2, 13
	v_mov_b32_e32 v145, v144
	v_pk_fma_f32 v[106:107], v[146:147], v[106:107], v[122:123]
	v_pk_fma_f32 v[104:105], v[142:143], v[104:105], v[120:121]
	v_add_u32_e32 v49, s14, v177
	ds_write_b128 v49, v[104:107]
	v_mov_b32_e32 v104, v144
	v_mov_b32_e32 v105, v144
	v_pk_mul_f32 v[120:121], v[50:51], v[144:145]
	v_mov_b32_e32 v144, 0
	v_mov_b32_e32 v145, 0
	v_mov_b32_e32 v146, 0
	v_mov_b32_e32 v147, 0
	v_pk_mul_f32 v[122:123], v[136:137], v[104:105]
	v_mov_b32_dpp v144, v12 row_shr:8 row_mask:0xf bank_mask:0xf
	v_mov_b32_dpp v145, v13 row_shr:8 row_mask:0xf bank_mask:0xf
	v_mov_b32_dpp v146, v14 row_shr:8 row_mask:0xf bank_mask:0xf
	v_mov_b32_dpp v147, v15 row_shr:8 row_mask:0xf bank_mask:0xf
	v_xor_b32_e32 v137, 0x80000000, v137
	v_xor_b32_e32 v136, 0x80000000, v136
	v_xor_b32_e32 v142, 0x80000000, v50
	v_xor_b32_e32 v143, 0x80000000, v51
	v_pk_fma_f32 v[120:121], v[12:13], v[130:131], v[120:121] neg_lo:[0,0,1] neg_hi:[0,0,1]
	v_pk_fma_f32 v[122:123], v[14:15], v[128:129], v[122:123] neg_lo:[0,0,1] neg_hi:[0,0,1]
	v_pk_mul_f32 v[128:129], v[136:137], v[146:147]
	v_pk_mul_f32 v[130:131], v[50:51], v[144:145] neg_lo:[1,0] neg_hi:[1,0]
	v_lshlrev_b32_e32 v116, 16, v96
	v_and_b32_e32 v117, 0xffff0000, v96
	v_lshlrev_b32_e32 v118, 16, v97
	v_and_b32_e32 v119, 0xffff0000, v97
	v_add_u32_e32 v148, s14, v169
	v_cndmask_b32_e64 v149, v129, v137, s[0:1]
	v_cndmask_b32_e64 v150, v128, v136, s[0:1]
	v_cndmask_b32_e64 v151, v131, v143, s[0:1]
	v_cndmask_b32_e64 v152, v130, v142, s[0:1]
	v_pk_mul_f32 v[128:129], v[120:121], v[144:145]
	v_pk_mul_f32 v[130:131], v[122:123], v[146:147]
	ds_write_b128 v148, v[116:119]
	v_mov_b32_e32 v104, 0
	v_mov_b32_e32 v107, 0
	v_mov_b32_e32 v106, 0
	v_mov_b32_e32 v105, 0
	v_mov_b32_e32 v116, 0
	v_mov_b32_e32 v119, 0
	v_mov_b32_e32 v118, 0
	v_mov_b32_e32 v117, 0
	v_cndmask_b32_e64 v131, v131, v123, s[0:1]
	v_cndmask_b32_e64 v153, v130, v122, s[0:1]
	v_cndmask_b32_e64 v130, v129, v121, s[0:1]
	v_cndmask_b32_e64 v154, v128, v120, s[0:1]
	v_mov_b32_dpp v104, v112 row_shr:8 row_mask:0xf bank_mask:0xf
	v_mov_b32_dpp v107, v108 row_shr:8 row_mask:0xf bank_mask:0xf
	v_mov_b32_dpp v106, v113 row_shr:8 row_mask:0xf bank_mask:0xf
	v_mov_b32_dpp v105, v109 row_shr:8 row_mask:0xf bank_mask:0xf
	v_mov_b32_dpp v116, v114 row_shr:8 row_mask:0xf bank_mask:0xf
	v_mov_b32_dpp v119, v110 row_shr:8 row_mask:0xf bank_mask:0xf
	v_mov_b32_dpp v118, v115 row_shr:8 row_mask:0xf bank_mask:0xf
	v_mov_b32_dpp v117, v111 row_shr:8 row_mask:0xf bank_mask:0xf
	v_cvt_pk_bf16_f32 v128, v152, v151
	v_cvt_pk_bf16_f32 v129, v150, v149
	v_cvt_pk_bf16_f32 v130, v154, v130
	v_cvt_pk_bf16_f32 v131, v153, v131
	v_add_u32_e32 v149, v193, v184
	v_lshrrev_b32_e32 v201, 2, v149
	v_bitop3_b32 v201, v201, v149, 64 bitop3:0x6c
	ds_write2_b64 v201, v[128:129], v[130:131] offset1:16
	s_and_saveexec_b64 s[14:15], s[4:5]
	s_cbranch_execz .LBB0_801
	v_pk_mul_f32 v[130:131], v[14:15], v[146:147]
	v_pk_mul_f32 v[128:129], v[12:13], v[144:145]
	ds_write_b128 v195, v[128:131] offset:16400
	v_mov_b32_e32 v128, v116
	v_mov_b32_e32 v129, v118
	v_pk_mul_f32 v[130:131], v[14:15], v[128:129]
	v_mov_b32_e32 v128, v104
	v_mov_b32_e32 v129, v106
	v_pk_mul_f32 v[128:129], v[12:13], v[128:129]
	ds_write_b128 v194, v[128:131] offset:32784
	v_mov_b32_e32 v128, v119
	v_mov_b32_e32 v129, v117
	v_pk_mul_f32 v[130:131], v[14:15], v[128:129]
	v_mov_b32_e32 v128, v107
	v_mov_b32_e32 v129, v105
	v_pk_mul_f32 v[128:129], v[12:13], v[128:129]
	v_xor_b32_e32 v203, 64, v194
	ds_write_b128 v203, v[128:131] offset:33040
	ds_write_b128 v194, v[112:115] offset:33296
	v_xor_b32_e32 v203, 64, v194
	ds_write_b128 v203, v[108:111] offset:33552
	v_pk_mul_f32 v[50:51], v[50:51], v[104:105] neg_lo:[1,0] neg_hi:[1,0]
	v_pk_mul_f32 v[108:109], v[136:137], v[116:117]
	v_pk_fma_f32 v[50:51], v[142:143], v[106:107], v[50:51] op_sel:[1,0,0] op_sel_hi:[0,1,1]
	v_pk_fma_f32 v[108:109], v[136:137], v[118:119], v[108:109] op_sel:[1,0,0] op_sel_hi:[0,1,1]
	v_pk_add_f32 v[50:51], v[50:51], v[108:109]
	s_nop 0
	v_pk_add_f32 v[140:141], v[140:141], v[50:51]
	v_pk_mul_f32 v[50:51], v[120:121], v[104:105]
	v_pk_mul_f32 v[104:105], v[122:123], v[116:117]
	v_pk_fma_f32 v[50:51], v[120:121], v[106:107], v[50:51] op_sel:[1,0,0] op_sel_hi:[0,1,1]
	v_pk_fma_f32 v[104:105], v[122:123], v[118:119], v[104:105] op_sel:[1,0,0] op_sel_hi:[0,1,1]
	v_pk_add_f32 v[50:51], v[50:51], v[104:105]
	s_nop 0
	v_pk_add_f32 v[138:139], v[138:139], v[50:51]

; #define LAS __attribute__((address_space(3)))
; __device__ __forceinline__ void scan_head(const Params& p, LAS unsigned char* lds, int bh, const int wave) {
;     ...
;             const int bp = chunk & 1, vb = chunk % 3;
;             const LAS unsigned char* awp = lds + L_AW + bp * 8192 + sel * 128 + rg * 16;
;             const LAS unsigned char* wwp = lds + L_W + bp * 8192 + rg * 16;
;             const LAS unsigned char* abp = lds + L_BK + bp * 16384 + rg * 256 + ri * 4;
;             const LAS unsigned char* vp = lds + L_V + vb * 8192 + (16 * wave + ri) * 4;
;             const LAS unsigned char* csp = lds + L_CS + bp * 256;
;             LAS unsigned char* yp = (rg == 0) ? (lds + L_Y + bp * 8192 + (16 * wave + ri) * 4) : ((rg == 2) ? (lds + L_Y + bp * 8192 + 256 + (16 * wave + ri) * 4) : (lds + L_DUMMY + tid * 4));
;             const int y_st = (rg & 1) ? 0 : 512;
;     ...
;             bf16x8 Pa0, Pa1, Qa0, Qa1; f32x4 Pw0, Pw1, Pw2, Pw3, Qw0, Qw1, Qw2, Qw3, Pcs, Qcs; float Pb0, Pb1, Pb2, Pb3, Pvt, Pvu, Qb0, Qb1, Qb2, Qb3, Qvt, Qvu;
;             SCAN_LD(P, 0);
; #pragma unroll 1
;             for (int pi = 0; pi < 16; pi += 2) {
;                 SCAN_LD(Q, pi + 1);
;                 SCAN_STEP(P, pi);
;                 if (pi + 2 < 16) SCAN_LD(P, pi + 2);
;                 SCAN_STEP(Q, pi + 1);
.LBB0_806:
	s_and_b64 vcc, exec, s[14:15]
	s_cbranch_vccz .LBB0_789
	s_setprio 3
	s_and_b32 s2, s51, 1
	s_lshl_b32 s15, s2, 13
	s_mul_i32 s14, s51, 0xab
	s_lshl_b32 s52, s2, 14
	s_bfe_u32 s14, s14, 0x70009
	s_lshl_b32 s44, s2, 8
	s_mul_i32 s14, s14, 3
	s_waitcnt vmcnt(0)
	s_sub_i32 s14, s51, s14
	s_and_b32 s14, s14, 0xff
	s_lshl_b32 s14, s14, 13
	s_add_i32 s44, s44, 0x20300
	v_add_u32_e32 v98, s15, v176
	v_add_u32_e32 v99, s15, v175
	v_add_u32_e32 v0, s52, v178
	v_add_u32_e32 v1, s14, v179
	v_add_u32_e32 v0, 0x8000, v0
	v_add_u32_e32 v4, 0x100, v1
	v_mov_b32_e32 v2, s44
	v_cndmask_b32_e64 v4, v4, v1, s[8:9]
	v_cndmask_b32_e64 v4, v4, v1, s[12:13]
	v_cndmask_b32_e64 v1, v4, v1, s[10:11]
	v_add_u32_e32 v4, s15, v181
	v_add_u32_e32 v6, 0xd00, v180
	v_add_u32_e32 v5, 0x100, v4
	v_cndmask_b32_e64 v5, v6, v5, s[10:11]
	v_cndmask_b32_e64 v3, v5, v4, s[8:9]
	v_lshrrev_b32_e32 v204, 2, v176
	v_and_b32_e32 v204, 64, v204
	v_sub_u32_e32 v205, v98, v204
	v_add_u32_e32 v98, v98, v204
	v_lshrrev_b32_e32 v206, 2, v178
	v_and_b32_e32 v206, 64, v206
	v_sub_u32_e32 v207, v0, v206
	v_add_u32_e32 v0, v0, v206
	ds_read_b128 v[68:71], v98 offset:0
	ds_read_b128 v[72:75], v205 offset:64
	ds_read_b128 v[76:79], v99 offset:16384
	ds_read_b128 v[80:83], v99 offset:16448
	ds_read_b128 v[84:87], v99 offset:16512
	ds_read_b128 v[88:91], v99 offset:16576
	ds_read_b32 v92, v0 offset:0
	ds_read_b32 v93, v207 offset:64
	ds_read_b32 v94, v0 offset:128
	ds_read_b32 v95, v207 offset:192
	ds_read_b32 v96, v1 offset:0
	ds_read_b128 v[100:103], v2 offset:0
	v_cvt_pk_bf16_f32 v8, v64, v65
	v_cvt_pk_bf16_f32 v9, v66, v67
	v_cvt_pk_bf16_f32 v10, v60, v61
	v_cvt_pk_bf16_f32 v11, v62, v63
	v_cvt_pk_bf16_f32 v12, v52, v53
	v_cvt_pk_bf16_f32 v13, v54, v55
	s_waitcnt lgkmcnt(7)
	v_mfma_f32_16x16x32_bf16 v[140:143], v[68:71], v[8:11], 0
	v_cvt_pk_bf16_f32 v14, v56, v57
	v_cvt_pk_bf16_f32 v15, v58, v59
	v_pk_mul_f32 v[64:65], v[64:65], v[76:77]
	v_pk_mul_f32 v[66:67], v[66:67], v[78:79]
	v_mfma_f32_16x16x32_bf16 v[140:143], v[72:75], v[12:15], v[140:143]
	v_pk_mul_f32 v[60:61], v[60:61], v[80:81]
	v_pk_mul_f32 v[62:63], v[62:63], v[82:83]
	v_pk_mul_f32 v[52:53], v[52:53], v[84:85]
	v_pk_mul_f32 v[54:55], v[54:55], v[86:87]
	s_waitcnt lgkmcnt(6)
	v_pk_mul_f32 v[56:57], v[56:57], v[88:89]
	v_pk_mul_f32 v[58:59], v[58:59], v[90:91]
	ds_read_b128 v[104:107], v98 offset:512
	ds_read_b128 v[108:111], v205 offset:576
	ds_read_b128 v[112:115], v99 offset:16640
	ds_read_b128 v[116:119], v99 offset:16704
	ds_read_b128 v[120:123], v99 offset:16768
	s_waitcnt lgkmcnt(5)
	v_fma_f32 v144, v100, v140, v142
	v_fmac_f32_e32 v144, v101, v96
	v_cndmask_b32_e64 v145, v96, v144, s[10:11]
	v_cndmask_b32_e64 v145, v145, v140, s[8:9]
	v_fma_f32 v50, v102, v140, v143
	v_fmac_f32_e32 v50, v103, v96
	v_mfma_f32_16x16x4_f32 v[64:67], v92, v145, v[64:67]
	v_mfma_f32_16x16x4_f32 v[60:63], v93, v145, v[60:63]
	v_mfma_f32_16x16x4_f32 v[52:55], v94, v145, v[52:55]
	v_mfma_f32_16x16x4_f32 v[56:59], v95, v145, v[56:59]
	v_cndmask_b32_e64 v50, v50, v141, s[8:9]
	ds_write_b32 v3, v50 offset:0
	ds_read_b128 v[128:131], v99 offset:16832
	ds_read_b32 v132, v0 offset:1024
	ds_read_b32 v133, v207 offset:1088
	ds_read_b32 v134, v0 offset:1152
	ds_read_b32 v135, v207 offset:1216
	ds_read_b32 v97, v1 offset:512
	ds_read_b128 v[136:139], v2 offset:16
	v_cvt_pk_bf16_f32 v8, v64, v65
	v_cvt_pk_bf16_f32 v9, v66, v67
	v_cvt_pk_bf16_f32 v10, v60, v61
	v_cvt_pk_bf16_f32 v11, v62, v63
	v_cvt_pk_bf16_f32 v12, v52, v53
	v_cvt_pk_bf16_f32 v13, v54, v55
	s_waitcnt lgkmcnt(7)
	v_mfma_f32_16x16x32_bf16 v[140:143], v[104:107], v[8:11], 0
	v_cvt_pk_bf16_f32 v14, v56, v57
	v_cvt_pk_bf16_f32 v15, v58, v59
	v_pk_mul_f32 v[64:65], v[64:65], v[112:113]
	v_pk_mul_f32 v[66:67], v[66:67], v[114:115]
	v_mfma_f32_16x16x32_bf16 v[140:143], v[108:111], v[12:15], v[140:143]
	v_pk_mul_f32 v[60:61], v[60:61], v[116:117]
	v_pk_mul_f32 v[62:63], v[62:63], v[118:119]
	v_pk_mul_f32 v[52:53], v[52:53], v[120:121]
	v_pk_mul_f32 v[54:55], v[54:55], v[122:123]
	s_waitcnt lgkmcnt(6)
	v_pk_mul_f32 v[56:57], v[56:57], v[128:129]
	v_pk_mul_f32 v[58:59], v[58:59], v[130:131]
	ds_read_b128 v[68:71], v98 offset:1024
	ds_read_b128 v[72:75], v205 offset:1088
	ds_read_b128 v[76:79], v99 offset:16896
	ds_read_b128 v[80:83], v99 offset:16960
	ds_read_b128 v[84:87], v99 offset:17024
	s_waitcnt lgkmcnt(5)
	v_fma_f32 v144, v136, v140, v142
	v_fmac_f32_e32 v144, v137, v97
	v_cndmask_b32_e64 v145, v97, v144, s[10:11]
	v_cndmask_b32_e64 v145, v145, v140, s[8:9]
	v_fma_f32 v50, v138, v140, v143
	v_fmac_f32_e32 v50, v139, v97
	v_mfma_f32_16x16x4_f32 v[64:67], v132, v145, v[64:67]
	v_mfma_f32_16x16x4_f32 v[60:63], v133, v145, v[60:63]
	v_mfma_f32_16x16x4_f32 v[52:55], v134, v145, v[52:55]
	v_mfma_f32_16x16x4_f32 v[56:59], v135, v145, v[56:59]
	v_cndmask_b32_e64 v50, v50, v141, s[8:9]
	ds_write_b32 v3, v50 offset:512
	ds_read_b128 v[88:91], v99 offset:17088
	ds_read_b32 v92, v0 offset:2048
	ds_read_b32 v93, v207 offset:2112
	ds_read_b32 v94, v0 offset:2176
	ds_read_b32 v95, v207 offset:2240
	ds_read_b32 v96, v1 offset:1024
	ds_read_b128 v[100:103], v2 offset:32
	v_cvt_pk_bf16_f32 v8, v64, v65
	v_cvt_pk_bf16_f32 v9, v66, v67
	v_cvt_pk_bf16_f32 v10, v60, v61
	v_cvt_pk_bf16_f32 v11, v62, v63
	v_cvt_pk_bf16_f32 v12, v52, v53
	v_cvt_pk_bf16_f32 v13, v54, v55
	s_waitcnt lgkmcnt(7)
	v_mfma_f32_16x16x32_bf16 v[140:143], v[68:71], v[8:11], 0
	v_cvt_pk_bf16_f32 v14, v56, v57
	v_cvt_pk_bf16_f32 v15, v58, v59
	v_pk_mul_f32 v[64:65], v[64:65], v[76:77]
	v_pk_mul_f32 v[66:67], v[66:67], v[78:79]
	v_mfma_f32_16x16x32_bf16 v[140:143], v[72:75], v[12:15], v[140:143]
	v_pk_mul_f32 v[60:61], v[60:61], v[80:81]
	v_pk_mul_f32 v[62:63], v[62:63], v[82:83]
	v_pk_mul_f32 v[52:53], v[52:53], v[84:85]
	v_pk_mul_f32 v[54:55], v[54:55], v[86:87]
	s_waitcnt lgkmcnt(6)
; __device__ __forceinline__ void scan_head(const Params& p, LAS unsigned char* lds, int bh, const int wave) {
;     ...
;             bf16x8 Pa0, Pa1, Qa0, Qa1; f32x4 Pw0, Pw1, Pw2, Pw3, Qw0, Qw1, Qw2, Qw3, Pcs, Qcs; float Pb0, Pb1, Pb2, Pb3, Pvt, Pvu, Qb0, Qb1, Qb2, Qb3, Qvt, Qvu;
;             SCAN_LD(P, 0);
; #pragma unroll 1
;             for (int pi = 0; pi < 16; pi += 2) {
;                 SCAN_LD(Q, pi + 1);
;                 SCAN_STEP(P, pi);
;                 if (pi + 2 < 16) SCAN_LD(P, pi + 2);
;                 SCAN_STEP(Q, pi + 1);
	v_pk_mul_f32 v[56:57], v[56:57], v[88:89]
	v_pk_mul_f32 v[58:59], v[58:59], v[90:91]
	ds_read_b128 v[104:107], v98 offset:1536
	ds_read_b128 v[108:111], v205 offset:1600
	ds_read_b128 v[112:115], v99 offset:17152
	ds_read_b128 v[116:119], v99 offset:17216
	ds_read_b128 v[120:123], v99 offset:17280
	s_waitcnt lgkmcnt(5)
	v_fma_f32 v144, v100, v140, v142
	v_fmac_f32_e32 v144, v101, v96
	v_cndmask_b32_e64 v145, v96, v144, s[10:11]
	v_cndmask_b32_e64 v145, v145, v140, s[8:9]
	v_fma_f32 v50, v102, v140, v143
	v_fmac_f32_e32 v50, v103, v96
	v_mfma_f32_16x16x4_f32 v[64:67], v92, v145, v[64:67]
	v_mfma_f32_16x16x4_f32 v[60:63], v93, v145, v[60:63]
	v_mfma_f32_16x16x4_f32 v[52:55], v94, v145, v[52:55]
	v_mfma_f32_16x16x4_f32 v[56:59], v95, v145, v[56:59]
	v_cndmask_b32_e64 v50, v50, v141, s[8:9]
	ds_write_b32 v3, v50 offset:1024
	ds_read_b128 v[128:131], v99 offset:17344
	ds_read_b32 v132, v0 offset:3072
	ds_read_b32 v133, v207 offset:3136
	ds_read_b32 v134, v0 offset:3200
	ds_read_b32 v135, v207 offset:3264
	ds_read_b32 v97, v1 offset:1536
	ds_read_b128 v[136:139], v2 offset:48
	v_cvt_pk_bf16_f32 v8, v64, v65
	v_cvt_pk_bf16_f32 v9, v66, v67
	v_cvt_pk_bf16_f32 v10, v60, v61
	v_cvt_pk_bf16_f32 v11, v62, v63
	v_cvt_pk_bf16_f32 v12, v52, v53
	v_cvt_pk_bf16_f32 v13, v54, v55
	s_waitcnt lgkmcnt(7)
	v_mfma_f32_16x16x32_bf16 v[140:143], v[104:107], v[8:11], 0
	v_cvt_pk_bf16_f32 v14, v56, v57
	v_cvt_pk_bf16_f32 v15, v58, v59
	v_pk_mul_f32 v[64:65], v[64:65], v[112:113]
	v_pk_mul_f32 v[66:67], v[66:67], v[114:115]
	v_mfma_f32_16x16x32_bf16 v[140:143], v[108:111], v[12:15], v[140:143]
	v_pk_mul_f32 v[60:61], v[60:61], v[116:117]
	v_pk_mul_f32 v[62:63], v[62:63], v[118:119]
	v_pk_mul_f32 v[52:53], v[52:53], v[120:121]
	v_pk_mul_f32 v[54:55], v[54:55], v[122:123]
	s_waitcnt lgkmcnt(6)
	v_pk_mul_f32 v[56:57], v[56:57], v[128:129]
	v_pk_mul_f32 v[58:59], v[58:59], v[130:131]
	ds_read_b128 v[68:71], v98 offset:2048
	ds_read_b128 v[72:75], v205 offset:2112
	ds_read_b128 v[76:79], v99 offset:17408
	ds_read_b128 v[80:83], v99 offset:17472
	ds_read_b128 v[84:87], v99 offset:17536
	s_waitcnt lgkmcnt(5)
	v_fma_f32 v144, v136, v140, v142
	v_fmac_f32_e32 v144, v137, v97
	v_cndmask_b32_e64 v145, v97, v144, s[10:11]
	v_cndmask_b32_e64 v145, v145, v140, s[8:9]
	v_fma_f32 v50, v138, v140, v143
	v_fmac_f32_e32 v50, v139, v97
	v_mfma_f32_16x16x4_f32 v[64:67], v132, v145, v[64:67]
	v_mfma_f32_16x16x4_f32 v[60:63], v133, v145, v[60:63]
	v_mfma_f32_16x16x4_f32 v[52:55], v134, v145, v[52:55]
	v_mfma_f32_16x16x4_f32 v[56:59], v135, v145, v[56:59]
	v_cndmask_b32_e64 v50, v50, v141, s[8:9]
	ds_write_b32 v3, v50 offset:1536
	ds_read_b128 v[88:91], v99 offset:17600
	ds_read_b32 v92, v0 offset:4096
	ds_read_b32 v93, v207 offset:4160
	ds_read_b32 v94, v0 offset:4224
	ds_read_b32 v95, v207 offset:4288
	ds_read_b32 v96, v1 offset:2048
	ds_read_b128 v[100:103], v2 offset:64
	v_cvt_pk_bf16_f32 v8, v64, v65
	v_cvt_pk_bf16_f32 v9, v66, v67
	v_cvt_pk_bf16_f32 v10, v60, v61
	v_cvt_pk_bf16_f32 v11, v62, v63
	v_cvt_pk_bf16_f32 v12, v52, v53
	v_cvt_pk_bf16_f32 v13, v54, v55
	s_waitcnt lgkmcnt(7)
	v_mfma_f32_16x16x32_bf16 v[140:143], v[68:71], v[8:11], 0
	v_cvt_pk_bf16_f32 v14, v56, v57
	v_cvt_pk_bf16_f32 v15, v58, v59
	v_pk_mul_f32 v[64:65], v[64:65], v[76:77]
	v_pk_mul_f32 v[66:67], v[66:67], v[78:79]
	v_mfma_f32_16x16x32_bf16 v[140:143], v[72:75], v[12:15], v[140:143]
	v_pk_mul_f32 v[60:61], v[60:61], v[80:81]
	v_pk_mul_f32 v[62:63], v[62:63], v[82:83]
	v_pk_mul_f32 v[52:53], v[52:53], v[84:85]
	v_pk_mul_f32 v[54:55], v[54:55], v[86:87]
	s_waitcnt lgkmcnt(6)
	v_pk_mul_f32 v[56:57], v[56:57], v[88:89]
	v_pk_mul_f32 v[58:59], v[58:59], v[90:91]
	ds_read_b128 v[104:107], v98 offset:2560
	ds_read_b128 v[108:111], v205 offset:2624
	ds_read_b128 v[112:115], v99 offset:17664
	ds_read_b128 v[116:119], v99 offset:17728
	ds_read_b128 v[120:123], v99 offset:17792
	s_waitcnt lgkmcnt(5)
	v_fma_f32 v144, v100, v140, v142
	v_fmac_f32_e32 v144, v101, v96
	v_cndmask_b32_e64 v145, v96, v144, s[10:11]
	v_cndmask_b32_e64 v145, v145, v140, s[8:9]
	v_fma_f32 v50, v102, v140, v143
	v_fmac_f32_e32 v50, v103, v96
	v_mfma_f32_16x16x4_f32 v[64:67], v92, v145, v[64:67]
	v_mfma_f32_16x16x4_f32 v[60:63], v93, v145, v[60:63]
	v_mfma_f32_16x16x4_f32 v[52:55], v94, v145, v[52:55]
	v_mfma_f32_16x16x4_f32 v[56:59], v95, v145, v[56:59]
	v_cndmask_b32_e64 v50, v50, v141, s[8:9]
	ds_write_b32 v3, v50 offset:2048
	ds_read_b128 v[128:131], v99 offset:17856
	ds_read_b32 v132, v0 offset:5120
	ds_read_b32 v133, v207 offset:5184
	ds_read_b32 v134, v0 offset:5248
	ds_read_b32 v135, v207 offset:5312
	ds_read_b32 v97, v1 offset:2560
	ds_read_b128 v[136:139], v2 offset:80
	v_cvt_pk_bf16_f32 v8, v64, v65
	v_cvt_pk_bf16_f32 v9, v66, v67
	v_cvt_pk_bf16_f32 v10, v60, v61
	v_cvt_pk_bf16_f32 v11, v62, v63
	v_cvt_pk_bf16_f32 v12, v52, v53
	v_cvt_pk_bf16_f32 v13, v54, v55
	s_waitcnt lgkmcnt(7)
	v_mfma_f32_16x16x32_bf16 v[140:143], v[104:107], v[8:11], 0
	v_cvt_pk_bf16_f32 v14, v56, v57
	v_cvt_pk_bf16_f32 v15, v58, v59
	v_pk_mul_f32 v[64:65], v[64:65], v[112:113]
	v_pk_mul_f32 v[66:67], v[66:67], v[114:115]
	v_mfma_f32_16x16x32_bf16 v[140:143], v[108:111], v[12:15], v[140:143]
	v_pk_mul_f32 v[60:61], v[60:61], v[116:117]
	v_pk_mul_f32 v[62:63], v[62:63], v[118:119]
	v_pk_mul_f32 v[52:53], v[52:53], v[120:121]
	v_pk_mul_f32 v[54:55], v[54:55], v[122:123]
	s_waitcnt lgkmcnt(6)
	v_pk_mul_f32 v[56:57], v[56:57], v[128:129]
	v_pk_mul_f32 v[58:59], v[58:59], v[130:131]
	ds_read_b128 v[68:71], v98 offset:3072
	ds_read_b128 v[72:75], v205 offset:3136
	ds_read_b128 v[76:79], v99 offset:17920
	ds_read_b128 v[80:83], v99 offset:17984
	ds_read_b128 v[84:87], v99 offset:18048
	s_waitcnt lgkmcnt(5)
; __device__ __forceinline__ void scan_head(const Params& p, LAS unsigned char* lds, int bh, const int wave) {
;     ...
;             bf16x8 Pa0, Pa1, Qa0, Qa1; f32x4 Pw0, Pw1, Pw2, Pw3, Qw0, Qw1, Qw2, Qw3, Pcs, Qcs; float Pb0, Pb1, Pb2, Pb3, Pvt, Pvu, Qb0, Qb1, Qb2, Qb3, Qvt, Qvu;
;             SCAN_LD(P, 0);
; #pragma unroll 1
;             for (int pi = 0; pi < 16; pi += 2) {
;                 SCAN_LD(Q, pi + 1);
;                 SCAN_STEP(P, pi);
;                 if (pi + 2 < 16) SCAN_LD(P, pi + 2);
;                 SCAN_STEP(Q, pi + 1);
	v_fma_f32 v144, v136, v140, v142
	v_fmac_f32_e32 v144, v137, v97
	v_cndmask_b32_e64 v145, v97, v144, s[10:11]
	v_cndmask_b32_e64 v145, v145, v140, s[8:9]
	v_fma_f32 v50, v138, v140, v143
	v_fmac_f32_e32 v50, v139, v97
	v_mfma_f32_16x16x4_f32 v[64:67], v132, v145, v[64:67]
	v_mfma_f32_16x16x4_f32 v[60:63], v133, v145, v[60:63]
	v_mfma_f32_16x16x4_f32 v[52:55], v134, v145, v[52:55]
	v_mfma_f32_16x16x4_f32 v[56:59], v135, v145, v[56:59]
	v_cndmask_b32_e64 v50, v50, v141, s[8:9]
	ds_write_b32 v3, v50 offset:2560
	ds_read_b128 v[88:91], v99 offset:18112
	ds_read_b32 v92, v0 offset:6144
	ds_read_b32 v93, v207 offset:6208
	ds_read_b32 v94, v0 offset:6272
	ds_read_b32 v95, v207 offset:6336
	ds_read_b32 v96, v1 offset:3072
	ds_read_b128 v[100:103], v2 offset:96
	v_cvt_pk_bf16_f32 v8, v64, v65
	v_cvt_pk_bf16_f32 v9, v66, v67
	v_cvt_pk_bf16_f32 v10, v60, v61
	v_cvt_pk_bf16_f32 v11, v62, v63
	v_cvt_pk_bf16_f32 v12, v52, v53
	v_cvt_pk_bf16_f32 v13, v54, v55
	s_waitcnt lgkmcnt(7)
	v_mfma_f32_16x16x32_bf16 v[140:143], v[68:71], v[8:11], 0
	v_cvt_pk_bf16_f32 v14, v56, v57
	v_cvt_pk_bf16_f32 v15, v58, v59
	v_pk_mul_f32 v[64:65], v[64:65], v[76:77]
	v_pk_mul_f32 v[66:67], v[66:67], v[78:79]
	v_mfma_f32_16x16x32_bf16 v[140:143], v[72:75], v[12:15], v[140:143]
	v_pk_mul_f32 v[60:61], v[60:61], v[80:81]
	v_pk_mul_f32 v[62:63], v[62:63], v[82:83]
	v_pk_mul_f32 v[52:53], v[52:53], v[84:85]
	v_pk_mul_f32 v[54:55], v[54:55], v[86:87]
	s_waitcnt lgkmcnt(6)
	v_pk_mul_f32 v[56:57], v[56:57], v[88:89]
	v_pk_mul_f32 v[58:59], v[58:59], v[90:91]
	ds_read_b128 v[104:107], v98 offset:3584
	ds_read_b128 v[108:111], v205 offset:3648
	ds_read_b128 v[112:115], v99 offset:18176
	ds_read_b128 v[116:119], v99 offset:18240
	ds_read_b128 v[120:123], v99 offset:18304
	s_waitcnt lgkmcnt(5)
	v_fma_f32 v144, v100, v140, v142
	v_fmac_f32_e32 v144, v101, v96
	v_cndmask_b32_e64 v145, v96, v144, s[10:11]
	v_cndmask_b32_e64 v145, v145, v140, s[8:9]
	v_fma_f32 v50, v102, v140, v143
	v_fmac_f32_e32 v50, v103, v96
	v_mfma_f32_16x16x4_f32 v[64:67], v92, v145, v[64:67]
	v_mfma_f32_16x16x4_f32 v[60:63], v93, v145, v[60:63]
	v_mfma_f32_16x16x4_f32 v[52:55], v94, v145, v[52:55]
	v_mfma_f32_16x16x4_f32 v[56:59], v95, v145, v[56:59]
	v_cndmask_b32_e64 v50, v50, v141, s[8:9]
	ds_write_b32 v3, v50 offset:3072
	ds_read_b128 v[128:131], v99 offset:18368
	ds_read_b32 v132, v0 offset:7168
	ds_read_b32 v133, v207 offset:7232
	ds_read_b32 v134, v0 offset:7296
	ds_read_b32 v135, v207 offset:7360
	ds_read_b32 v97, v1 offset:3584
	ds_read_b128 v[136:139], v2 offset:112
	v_cvt_pk_bf16_f32 v8, v64, v65
	v_cvt_pk_bf16_f32 v9, v66, v67
	v_cvt_pk_bf16_f32 v10, v60, v61
	v_cvt_pk_bf16_f32 v11, v62, v63
	v_cvt_pk_bf16_f32 v12, v52, v53
	v_cvt_pk_bf16_f32 v13, v54, v55
	s_waitcnt lgkmcnt(7)
	v_mfma_f32_16x16x32_bf16 v[140:143], v[104:107], v[8:11], 0
	v_cvt_pk_bf16_f32 v14, v56, v57
	v_cvt_pk_bf16_f32 v15, v58, v59
	v_pk_mul_f32 v[64:65], v[64:65], v[112:113]
	v_pk_mul_f32 v[66:67], v[66:67], v[114:115]
	v_mfma_f32_16x16x32_bf16 v[140:143], v[108:111], v[12:15], v[140:143]
	v_pk_mul_f32 v[60:61], v[60:61], v[116:117]
	v_pk_mul_f32 v[62:63], v[62:63], v[118:119]
	v_pk_mul_f32 v[52:53], v[52:53], v[120:121]
	v_pk_mul_f32 v[54:55], v[54:55], v[122:123]
	s_waitcnt lgkmcnt(6)
	v_pk_mul_f32 v[56:57], v[56:57], v[128:129]
	v_pk_mul_f32 v[58:59], v[58:59], v[130:131]
	ds_read_b128 v[68:71], v98 offset:4096
	ds_read_b128 v[72:75], v205 offset:4160
	ds_read_b128 v[76:79], v99 offset:18432
	ds_read_b128 v[80:83], v99 offset:18496
	ds_read_b128 v[84:87], v99 offset:18560
	s_waitcnt lgkmcnt(5)
	v_fma_f32 v144, v136, v140, v142
	v_fmac_f32_e32 v144, v137, v97
	v_cndmask_b32_e64 v145, v97, v144, s[10:11]
	v_cndmask_b32_e64 v145, v145, v140, s[8:9]
	v_fma_f32 v50, v138, v140, v143
	v_fmac_f32_e32 v50, v139, v97
	v_mfma_f32_16x16x4_f32 v[64:67], v132, v145, v[64:67]
	v_mfma_f32_16x16x4_f32 v[60:63], v133, v145, v[60:63]
	v_mfma_f32_16x16x4_f32 v[52:55], v134, v145, v[52:55]
	v_mfma_f32_16x16x4_f32 v[56:59], v135, v145, v[56:59]
	v_cndmask_b32_e64 v50, v50, v141, s[8:9]
	ds_write_b32 v3, v50 offset:3584
	ds_read_b128 v[88:91], v99 offset:18624
	ds_read_b32 v92, v0 offset:8192
	ds_read_b32 v93, v207 offset:8256
	ds_read_b32 v94, v0 offset:8320
	ds_read_b32 v95, v207 offset:8384
	ds_read_b32 v96, v1 offset:4096
	ds_read_b128 v[100:103], v2 offset:128
	v_cvt_pk_bf16_f32 v8, v64, v65
	v_cvt_pk_bf16_f32 v9, v66, v67
	v_cvt_pk_bf16_f32 v10, v60, v61
	v_cvt_pk_bf16_f32 v11, v62, v63
	v_cvt_pk_bf16_f32 v12, v52, v53
	v_cvt_pk_bf16_f32 v13, v54, v55
	s_waitcnt lgkmcnt(7)
	v_mfma_f32_16x16x32_bf16 v[140:143], v[68:71], v[8:11], 0
	v_cvt_pk_bf16_f32 v14, v56, v57
	v_cvt_pk_bf16_f32 v15, v58, v59
	v_pk_mul_f32 v[64:65], v[64:65], v[76:77]
	v_pk_mul_f32 v[66:67], v[66:67], v[78:79]
	v_mfma_f32_16x16x32_bf16 v[140:143], v[72:75], v[12:15], v[140:143]
	v_pk_mul_f32 v[60:61], v[60:61], v[80:81]
	v_pk_mul_f32 v[62:63], v[62:63], v[82:83]
	v_pk_mul_f32 v[52:53], v[52:53], v[84:85]
	v_pk_mul_f32 v[54:55], v[54:55], v[86:87]
	s_waitcnt lgkmcnt(6)
	v_pk_mul_f32 v[56:57], v[56:57], v[88:89]
	v_pk_mul_f32 v[58:59], v[58:59], v[90:91]
	ds_read_b128 v[104:107], v98 offset:4608
	ds_read_b128 v[108:111], v205 offset:4672
	ds_read_b128 v[112:115], v99 offset:18688
	ds_read_b128 v[116:119], v99 offset:18752
	ds_read_b128 v[120:123], v99 offset:18816
	s_waitcnt lgkmcnt(5)
; __device__ __forceinline__ void scan_head(const Params& p, LAS unsigned char* lds, int bh, const int wave) {
;     ...
;             bf16x8 Pa0, Pa1, Qa0, Qa1; f32x4 Pw0, Pw1, Pw2, Pw3, Qw0, Qw1, Qw2, Qw3, Pcs, Qcs; float Pb0, Pb1, Pb2, Pb3, Pvt, Pvu, Qb0, Qb1, Qb2, Qb3, Qvt, Qvu;
;             SCAN_LD(P, 0);
; #pragma unroll 1
;             for (int pi = 0; pi < 16; pi += 2) {
;                 SCAN_LD(Q, pi + 1);
;                 SCAN_STEP(P, pi);
;                 if (pi + 2 < 16) SCAN_LD(P, pi + 2);
;                 SCAN_STEP(Q, pi + 1);
	v_fma_f32 v144, v100, v140, v142
	v_fmac_f32_e32 v144, v101, v96
	v_cndmask_b32_e64 v145, v96, v144, s[10:11]
	v_cndmask_b32_e64 v145, v145, v140, s[8:9]
	v_fma_f32 v50, v102, v140, v143
	v_fmac_f32_e32 v50, v103, v96
	v_mfma_f32_16x16x4_f32 v[64:67], v92, v145, v[64:67]
	v_mfma_f32_16x16x4_f32 v[60:63], v93, v145, v[60:63]
	v_mfma_f32_16x16x4_f32 v[52:55], v94, v145, v[52:55]
	v_mfma_f32_16x16x4_f32 v[56:59], v95, v145, v[56:59]
	v_cndmask_b32_e64 v50, v50, v141, s[8:9]
	ds_write_b32 v3, v50 offset:4096
	ds_read_b128 v[128:131], v99 offset:18880
	ds_read_b32 v132, v0 offset:9216
	ds_read_b32 v133, v207 offset:9280
	ds_read_b32 v134, v0 offset:9344
	ds_read_b32 v135, v207 offset:9408
	ds_read_b32 v97, v1 offset:4608
	ds_read_b128 v[136:139], v2 offset:144
	v_cvt_pk_bf16_f32 v8, v64, v65
	v_cvt_pk_bf16_f32 v9, v66, v67
	v_cvt_pk_bf16_f32 v10, v60, v61
	v_cvt_pk_bf16_f32 v11, v62, v63
	v_cvt_pk_bf16_f32 v12, v52, v53
	v_cvt_pk_bf16_f32 v13, v54, v55
	s_waitcnt lgkmcnt(7)
	v_mfma_f32_16x16x32_bf16 v[140:143], v[104:107], v[8:11], 0
	v_cvt_pk_bf16_f32 v14, v56, v57
	v_cvt_pk_bf16_f32 v15, v58, v59
	v_pk_mul_f32 v[64:65], v[64:65], v[112:113]
	v_pk_mul_f32 v[66:67], v[66:67], v[114:115]
	v_mfma_f32_16x16x32_bf16 v[140:143], v[108:111], v[12:15], v[140:143]
	v_pk_mul_f32 v[60:61], v[60:61], v[116:117]
	v_pk_mul_f32 v[62:63], v[62:63], v[118:119]
	v_pk_mul_f32 v[52:53], v[52:53], v[120:121]
	v_pk_mul_f32 v[54:55], v[54:55], v[122:123]
	s_waitcnt lgkmcnt(6)
	v_pk_mul_f32 v[56:57], v[56:57], v[128:129]
	v_pk_mul_f32 v[58:59], v[58:59], v[130:131]
	ds_read_b128 v[68:71], v98 offset:5120
	ds_read_b128 v[72:75], v205 offset:5184
	ds_read_b128 v[76:79], v99 offset:18944
	ds_read_b128 v[80:83], v99 offset:19008
	ds_read_b128 v[84:87], v99 offset:19072
	s_waitcnt lgkmcnt(5)
	v_fma_f32 v144, v136, v140, v142
	v_fmac_f32_e32 v144, v137, v97
	v_cndmask_b32_e64 v145, v97, v144, s[10:11]
	v_cndmask_b32_e64 v145, v145, v140, s[8:9]
	v_fma_f32 v50, v138, v140, v143
	v_fmac_f32_e32 v50, v139, v97
	v_mfma_f32_16x16x4_f32 v[64:67], v132, v145, v[64:67]
	v_mfma_f32_16x16x4_f32 v[60:63], v133, v145, v[60:63]
	v_mfma_f32_16x16x4_f32 v[52:55], v134, v145, v[52:55]
	v_mfma_f32_16x16x4_f32 v[56:59], v135, v145, v[56:59]
	v_cndmask_b32_e64 v50, v50, v141, s[8:9]
	ds_write_b32 v3, v50 offset:4608
	ds_read_b128 v[88:91], v99 offset:19136
	ds_read_b32 v92, v0 offset:10240
	ds_read_b32 v93, v207 offset:10304
	ds_read_b32 v94, v0 offset:10368
	ds_read_b32 v95, v207 offset:10432
	ds_read_b32 v96, v1 offset:5120
	ds_read_b128 v[100:103], v2 offset:160
	v_cvt_pk_bf16_f32 v8, v64, v65
	v_cvt_pk_bf16_f32 v9, v66, v67
	v_cvt_pk_bf16_f32 v10, v60, v61
	v_cvt_pk_bf16_f32 v11, v62, v63
	v_cvt_pk_bf16_f32 v12, v52, v53
	v_cvt_pk_bf16_f32 v13, v54, v55
	s_waitcnt lgkmcnt(7)
	v_mfma_f32_16x16x32_bf16 v[140:143], v[68:71], v[8:11], 0
	v_cvt_pk_bf16_f32 v14, v56, v57
	v_cvt_pk_bf16_f32 v15, v58, v59
	v_pk_mul_f32 v[64:65], v[64:65], v[76:77]
	v_pk_mul_f32 v[66:67], v[66:67], v[78:79]
	v_mfma_f32_16x16x32_bf16 v[140:143], v[72:75], v[12:15], v[140:143]
	v_pk_mul_f32 v[60:61], v[60:61], v[80:81]
	v_pk_mul_f32 v[62:63], v[62:63], v[82:83]
	v_pk_mul_f32 v[52:53], v[52:53], v[84:85]
	v_pk_mul_f32 v[54:55], v[54:55], v[86:87]
	s_waitcnt lgkmcnt(6)
	v_pk_mul_f32 v[56:57], v[56:57], v[88:89]
	v_pk_mul_f32 v[58:59], v[58:59], v[90:91]
	ds_read_b128 v[104:107], v98 offset:5632
	ds_read_b128 v[108:111], v205 offset:5696
	ds_read_b128 v[112:115], v99 offset:19200
	ds_read_b128 v[116:119], v99 offset:19264
	ds_read_b128 v[120:123], v99 offset:19328
	s_waitcnt lgkmcnt(5)
	v_fma_f32 v144, v100, v140, v142
	v_fmac_f32_e32 v144, v101, v96
	v_cndmask_b32_e64 v145, v96, v144, s[10:11]
	v_cndmask_b32_e64 v145, v145, v140, s[8:9]
	v_fma_f32 v50, v102, v140, v143
	v_fmac_f32_e32 v50, v103, v96
	v_mfma_f32_16x16x4_f32 v[64:67], v92, v145, v[64:67]
	v_mfma_f32_16x16x4_f32 v[60:63], v93, v145, v[60:63]
	v_mfma_f32_16x16x4_f32 v[52:55], v94, v145, v[52:55]
	v_mfma_f32_16x16x4_f32 v[56:59], v95, v145, v[56:59]
	v_cndmask_b32_e64 v50, v50, v141, s[8:9]
	ds_write_b32 v3, v50 offset:5120
	ds_read_b128 v[128:131], v99 offset:19392
	ds_read_b32 v132, v0 offset:11264
	ds_read_b32 v133, v207 offset:11328
	ds_read_b32 v134, v0 offset:11392
	ds_read_b32 v135, v207 offset:11456
	ds_read_b32 v97, v1 offset:5632
	ds_read_b128 v[136:139], v2 offset:176
	v_cvt_pk_bf16_f32 v8, v64, v65
	v_cvt_pk_bf16_f32 v9, v66, v67
	v_cvt_pk_bf16_f32 v10, v60, v61
	v_cvt_pk_bf16_f32 v11, v62, v63
	v_cvt_pk_bf16_f32 v12, v52, v53
	v_cvt_pk_bf16_f32 v13, v54, v55
	s_waitcnt lgkmcnt(7)
	v_mfma_f32_16x16x32_bf16 v[140:143], v[104:107], v[8:11], 0
	v_cvt_pk_bf16_f32 v14, v56, v57
	v_cvt_pk_bf16_f32 v15, v58, v59
	v_pk_mul_f32 v[64:65], v[64:65], v[112:113]
	v_pk_mul_f32 v[66:67], v[66:67], v[114:115]
	v_mfma_f32_16x16x32_bf16 v[140:143], v[108:111], v[12:15], v[140:143]
	v_pk_mul_f32 v[60:61], v[60:61], v[116:117]
	v_pk_mul_f32 v[62:63], v[62:63], v[118:119]
	v_pk_mul_f32 v[52:53], v[52:53], v[120:121]
	v_pk_mul_f32 v[54:55], v[54:55], v[122:123]
	s_waitcnt lgkmcnt(6)
	v_pk_mul_f32 v[56:57], v[56:57], v[128:129]
	v_pk_mul_f32 v[58:59], v[58:59], v[130:131]
	ds_read_b128 v[68:71], v98 offset:6144
	ds_read_b128 v[72:75], v205 offset:6208
	ds_read_b128 v[76:79], v99 offset:19456
	ds_read_b128 v[80:83], v99 offset:19520
	ds_read_b128 v[84:87], v99 offset:19584
	s_waitcnt lgkmcnt(5)
; __device__ __forceinline__ void scan_head(const Params& p, LAS unsigned char* lds, int bh, const int wave) {
;     ...
;             bf16x8 Pa0, Pa1, Qa0, Qa1; f32x4 Pw0, Pw1, Pw2, Pw3, Qw0, Qw1, Qw2, Qw3, Pcs, Qcs; float Pb0, Pb1, Pb2, Pb3, Pvt, Pvu, Qb0, Qb1, Qb2, Qb3, Qvt, Qvu;
;             SCAN_LD(P, 0);
; #pragma unroll 1
;             for (int pi = 0; pi < 16; pi += 2) {
;                 SCAN_LD(Q, pi + 1);
;                 SCAN_STEP(P, pi);
;                 if (pi + 2 < 16) SCAN_LD(P, pi + 2);
;                 SCAN_STEP(Q, pi + 1);
	v_fma_f32 v144, v136, v140, v142
	v_fmac_f32_e32 v144, v137, v97
	v_cndmask_b32_e64 v145, v97, v144, s[10:11]
	v_cndmask_b32_e64 v145, v145, v140, s[8:9]
	v_fma_f32 v50, v138, v140, v143
	v_fmac_f32_e32 v50, v139, v97
	v_mfma_f32_16x16x4_f32 v[64:67], v132, v145, v[64:67]
	v_mfma_f32_16x16x4_f32 v[60:63], v133, v145, v[60:63]
	v_mfma_f32_16x16x4_f32 v[52:55], v134, v145, v[52:55]
	v_mfma_f32_16x16x4_f32 v[56:59], v135, v145, v[56:59]
	v_cndmask_b32_e64 v50, v50, v141, s[8:9]
	ds_write_b32 v3, v50 offset:5632
	ds_read_b128 v[88:91], v99 offset:19648
	ds_read_b32 v92, v0 offset:12288
	ds_read_b32 v93, v207 offset:12352
	ds_read_b32 v94, v0 offset:12416
	ds_read_b32 v95, v207 offset:12480
	ds_read_b32 v96, v1 offset:6144
	ds_read_b128 v[100:103], v2 offset:192
	v_cvt_pk_bf16_f32 v8, v64, v65
	v_cvt_pk_bf16_f32 v9, v66, v67
	v_cvt_pk_bf16_f32 v10, v60, v61
	v_cvt_pk_bf16_f32 v11, v62, v63
	v_cvt_pk_bf16_f32 v12, v52, v53
	v_cvt_pk_bf16_f32 v13, v54, v55
	s_waitcnt lgkmcnt(7)
	v_mfma_f32_16x16x32_bf16 v[140:143], v[68:71], v[8:11], 0
	v_cvt_pk_bf16_f32 v14, v56, v57
	v_cvt_pk_bf16_f32 v15, v58, v59
	v_pk_mul_f32 v[64:65], v[64:65], v[76:77]
	v_pk_mul_f32 v[66:67], v[66:67], v[78:79]
	v_mfma_f32_16x16x32_bf16 v[140:143], v[72:75], v[12:15], v[140:143]
	v_pk_mul_f32 v[60:61], v[60:61], v[80:81]
	v_pk_mul_f32 v[62:63], v[62:63], v[82:83]
	v_pk_mul_f32 v[52:53], v[52:53], v[84:85]
	v_pk_mul_f32 v[54:55], v[54:55], v[86:87]
	s_waitcnt lgkmcnt(6)
	v_pk_mul_f32 v[56:57], v[56:57], v[88:89]
	v_pk_mul_f32 v[58:59], v[58:59], v[90:91]
	ds_read_b128 v[104:107], v98 offset:6656
	ds_read_b128 v[108:111], v205 offset:6720
	ds_read_b128 v[112:115], v99 offset:19712
	ds_read_b128 v[116:119], v99 offset:19776
	ds_read_b128 v[120:123], v99 offset:19840
	s_waitcnt lgkmcnt(5)
	v_fma_f32 v144, v100, v140, v142
	v_fmac_f32_e32 v144, v101, v96
	v_cndmask_b32_e64 v145, v96, v144, s[10:11]
	v_cndmask_b32_e64 v145, v145, v140, s[8:9]
	v_fma_f32 v50, v102, v140, v143
	v_fmac_f32_e32 v50, v103, v96
	v_mfma_f32_16x16x4_f32 v[64:67], v92, v145, v[64:67]
	v_mfma_f32_16x16x4_f32 v[60:63], v93, v145, v[60:63]
	v_mfma_f32_16x16x4_f32 v[52:55], v94, v145, v[52:55]
	v_mfma_f32_16x16x4_f32 v[56:59], v95, v145, v[56:59]
	v_cndmask_b32_e64 v50, v50, v141, s[8:9]
	ds_write_b32 v3, v50 offset:6144
	ds_read_b128 v[128:131], v99 offset:19904
	ds_read_b32 v132, v0 offset:13312
	ds_read_b32 v133, v207 offset:13376
	ds_read_b32 v134, v0 offset:13440
	ds_read_b32 v135, v207 offset:13504
	ds_read_b32 v97, v1 offset:6656
	ds_read_b128 v[136:139], v2 offset:208
	v_cvt_pk_bf16_f32 v8, v64, v65
	v_cvt_pk_bf16_f32 v9, v66, v67
	v_cvt_pk_bf16_f32 v10, v60, v61
	v_cvt_pk_bf16_f32 v11, v62, v63
	v_cvt_pk_bf16_f32 v12, v52, v53
	v_cvt_pk_bf16_f32 v13, v54, v55
	s_waitcnt lgkmcnt(7)
	v_mfma_f32_16x16x32_bf16 v[140:143], v[104:107], v[8:11], 0
	v_cvt_pk_bf16_f32 v14, v56, v57
	v_cvt_pk_bf16_f32 v15, v58, v59
	v_pk_mul_f32 v[64:65], v[64:65], v[112:113]
	v_pk_mul_f32 v[66:67], v[66:67], v[114:115]
	v_mfma_f32_16x16x32_bf16 v[140:143], v[108:111], v[12:15], v[140:143]
	v_pk_mul_f32 v[60:61], v[60:61], v[116:117]
	v_pk_mul_f32 v[62:63], v[62:63], v[118:119]
	v_pk_mul_f32 v[52:53], v[52:53], v[120:121]
	v_pk_mul_f32 v[54:55], v[54:55], v[122:123]
	s_waitcnt lgkmcnt(6)
	v_pk_mul_f32 v[56:57], v[56:57], v[128:129]
	v_pk_mul_f32 v[58:59], v[58:59], v[130:131]
	ds_read_b128 v[68:71], v98 offset:7168
	ds_read_b128 v[72:75], v205 offset:7232
	ds_read_b128 v[76:79], v99 offset:19968
	ds_read_b128 v[80:83], v99 offset:20032
	ds_read_b128 v[84:87], v99 offset:20096
	s_waitcnt lgkmcnt(5)
; __device__ __forceinline__ void scan_head(const Params& p, LAS unsigned char* lds, int bh, const int wave) {
;     ...
;             bf16x8 Pa0, Pa1, Qa0, Qa1; f32x4 Pw0, Pw1, Pw2, Pw3, Qw0, Qw1, Qw2, Qw3, Pcs, Qcs; float Pb0, Pb1, Pb2, Pb3, Pvt, Pvu, Qb0, Qb1, Qb2, Qb3, Qvt, Qvu;
;             SCAN_LD(P, 0);
; #pragma unroll 1
;             for (int pi = 0; pi < 16; pi += 2) {
;                 SCAN_LD(Q, pi + 1);
;                 SCAN_STEP(P, pi);
;                 if (pi + 2 < 16) SCAN_LD(P, pi + 2);
;                 SCAN_STEP(Q, pi + 1);
	v_fma_f32 v144, v136, v140, v142
	v_fmac_f32_e32 v144, v137, v97
	v_cndmask_b32_e64 v145, v97, v144, s[10:11]
	v_cndmask_b32_e64 v145, v145, v140, s[8:9]
	v_fma_f32 v50, v138, v140, v143
	v_fmac_f32_e32 v50, v139, v97
	v_mfma_f32_16x16x4_f32 v[64:67], v132, v145, v[64:67]
	v_mfma_f32_16x16x4_f32 v[60:63], v133, v145, v[60:63]
	v_mfma_f32_16x16x4_f32 v[52:55], v134, v145, v[52:55]
	v_mfma_f32_16x16x4_f32 v[56:59], v135, v145, v[56:59]
	v_cndmask_b32_e64 v50, v50, v141, s[8:9]
	ds_write_b32 v3, v50 offset:6656
	ds_read_b128 v[88:91], v99 offset:20160
	ds_read_b32 v92, v0 offset:14336
	ds_read_b32 v93, v207 offset:14400
	ds_read_b32 v94, v0 offset:14464
	ds_read_b32 v95, v207 offset:14528
	ds_read_b32 v96, v1 offset:7168
	ds_read_b128 v[100:103], v2 offset:224
	v_cvt_pk_bf16_f32 v8, v64, v65
	v_cvt_pk_bf16_f32 v9, v66, v67
	v_cvt_pk_bf16_f32 v10, v60, v61
	v_cvt_pk_bf16_f32 v11, v62, v63
	v_cvt_pk_bf16_f32 v12, v52, v53
	v_cvt_pk_bf16_f32 v13, v54, v55
	s_waitcnt lgkmcnt(7)
	v_mfma_f32_16x16x32_bf16 v[140:143], v[68:71], v[8:11], 0
	v_cvt_pk_bf16_f32 v14, v56, v57
	v_cvt_pk_bf16_f32 v15, v58, v59
	v_pk_mul_f32 v[64:65], v[64:65], v[76:77]
	v_pk_mul_f32 v[66:67], v[66:67], v[78:79]
	v_mfma_f32_16x16x32_bf16 v[140:143], v[72:75], v[12:15], v[140:143]
	v_pk_mul_f32 v[60:61], v[60:61], v[80:81]
	v_pk_mul_f32 v[62:63], v[62:63], v[82:83]
	v_pk_mul_f32 v[52:53], v[52:53], v[84:85]
	v_pk_mul_f32 v[54:55], v[54:55], v[86:87]
	s_waitcnt lgkmcnt(6)
	v_pk_mul_f32 v[56:57], v[56:57], v[88:89]
	v_pk_mul_f32 v[58:59], v[58:59], v[90:91]
	ds_read_b128 v[104:107], v98 offset:7680
	ds_read_b128 v[108:111], v205 offset:7744
	ds_read_b128 v[112:115], v99 offset:20224
	ds_read_b128 v[116:119], v99 offset:20288
	ds_read_b128 v[120:123], v99 offset:20352
	s_waitcnt lgkmcnt(5)
	v_fma_f32 v144, v100, v140, v142
	v_fmac_f32_e32 v144, v101, v96
	v_cndmask_b32_e64 v145, v96, v144, s[10:11]
	v_cndmask_b32_e64 v145, v145, v140, s[8:9]
	v_fma_f32 v50, v102, v140, v143
	v_fmac_f32_e32 v50, v103, v96
	v_mfma_f32_16x16x4_f32 v[64:67], v92, v145, v[64:67]
	v_mfma_f32_16x16x4_f32 v[60:63], v93, v145, v[60:63]
	v_mfma_f32_16x16x4_f32 v[52:55], v94, v145, v[52:55]
	v_mfma_f32_16x16x4_f32 v[56:59], v95, v145, v[56:59]
	v_cndmask_b32_e64 v50, v50, v141, s[8:9]
	ds_write_b32 v3, v50 offset:7168
	ds_read_b128 v[128:131], v99 offset:20416
	ds_read_b32 v132, v0 offset:15360
	ds_read_b32 v133, v207 offset:15424
	ds_read_b32 v134, v0 offset:15488
	ds_read_b32 v135, v207 offset:15552
	ds_read_b32 v97, v1 offset:7680
	ds_read_b128 v[136:139], v2 offset:240
	v_cvt_pk_bf16_f32 v8, v64, v65
	v_cvt_pk_bf16_f32 v9, v66, v67
	v_cvt_pk_bf16_f32 v10, v60, v61
	v_cvt_pk_bf16_f32 v11, v62, v63
	v_cvt_pk_bf16_f32 v12, v52, v53
	v_cvt_pk_bf16_f32 v13, v54, v55
	s_waitcnt lgkmcnt(7)
	v_mfma_f32_16x16x32_bf16 v[140:143], v[104:107], v[8:11], 0
	v_cvt_pk_bf16_f32 v14, v56, v57
	v_cvt_pk_bf16_f32 v15, v58, v59
	v_pk_mul_f32 v[64:65], v[64:65], v[112:113]
	v_pk_mul_f32 v[66:67], v[66:67], v[114:115]
	v_mfma_f32_16x16x32_bf16 v[140:143], v[108:111], v[12:15], v[140:143]
	v_pk_mul_f32 v[60:61], v[60:61], v[116:117]
	v_pk_mul_f32 v[62:63], v[62:63], v[118:119]
	v_pk_mul_f32 v[52:53], v[52:53], v[120:121]
	v_pk_mul_f32 v[54:55], v[54:55], v[122:123]
	s_waitcnt lgkmcnt(6)
	v_pk_mul_f32 v[56:57], v[56:57], v[128:129]
	v_pk_mul_f32 v[58:59], v[58:59], v[130:131]
	s_waitcnt lgkmcnt(0)
	s_nop 1
	v_fma_f32 v144, v136, v140, v142
	v_fmac_f32_e32 v144, v137, v97
	v_cndmask_b32_e64 v145, v97, v144, s[10:11]
	v_cndmask_b32_e64 v145, v145, v140, s[8:9]
	v_fma_f32 v50, v138, v140, v143
	v_fmac_f32_e32 v50, v139, v97
	v_mfma_f32_16x16x4_f32 v[64:67], v132, v145, v[64:67]
	v_mfma_f32_16x16x4_f32 v[60:63], v133, v145, v[60:63]
	v_mfma_f32_16x16x4_f32 v[52:55], v134, v145, v[52:55]
	v_mfma_f32_16x16x4_f32 v[56:59], v135, v145, v[56:59]
	v_cndmask_b32_e64 v50, v50, v141, s[8:9]
	ds_write_b32 v3, v50 offset:7680
	s_nop 7
